# latent attention body rewritten around v_mfma_f32_16x16x32_bf16 (one tile per trip, K fragment shared by both query tiles, counted LDS waits), max-free softmax with gain guard + original loop fallback
# speedup vs baseline: 1.0606x; 1.0135x over previous
; __device__ __forceinline__ int otid() { int t = threadIdx.x; asm volatile("" : "+v"(t)); return t; }
; __device__ __forceinline__ void attn_dma_body(const bf16_t* __restrict__ Qb, int ldq, int tpos0, const float* __restrict__ rope, const float* __restrict__ qgain, ...
;   const int tid = otid(), wid = tid >> 6, lane = tid & 63, r32 = lane & 31, hi = lane >> 5;
;   float* ws = (float*)(lds + TAB_OFF + 1024) + wid * 64; float* li_l = ws; float* al_l = ws + 32;
;   float m_reg = -1e30f, l_reg = 0; f32x16 o[4] = {}; bf16x8 qr[8];
;   const bf16_t* Qw = Qb + (long)(wid * QBLK + r32) * ldq + hi * 8;
;   unsigned koff[2], voff[2];
; #pragma unroll
;   for (int c = 0; c < 2; ++c) { const int g = c * 512 + tid;
;     { const int row = g >> 4, ch = (g & 15) ^ (row & 7); koff[c] = (unsigned)(row * 128 + ch * 8) * 2u; }
;     { const int sub = g >> 5, kk = (sub >> 2) * 8 + ((g >> 2) & 7), k = (kk & ~0xC) | ((kk & 4) << 1) | ((kk & 8) >> 1), col = (sub & 3) * 32 + (g & 3) * 8; voff[c] = (unsigned)(k * 128 + col) * 2u; } }
;   const unsigned wbase = (unsigned)__builtin_amdgcn_readfirstlane(wid) * 1024u;
;   typedef __attribute__((address_space(3))) unsigned lds_u32;
;   lds_u32* ldsl = (lds_u32*)(__attribute__((address_space(3))) char*)lds;
;     ...
;   const int NT = seq / KVBLK;
;   ATT_DMA(0, 0); ATT_DMA(1, 1);
; #pragma unroll
;   for (int d0 = 0; d0 < 8; ++d0) qr[d0] = ld8(Qw + d0 * 16);
;   if (tpos0 >= 0) {
;     float ss = 0.f;
; #pragma unroll
;     for (int d0 = 0; d0 < 8; ++d0)
; #pragma unroll
;       for (int i = 0; i < 8; ++i) { const float x = bf2f((unsigned)(unsigned short)qr[d0][i]); ss += x * x; }
;     { auto rr = __builtin_amdgcn_permlane32_swap(__float_as_uint(ss), __float_as_uint(ss), false, false); ss = __uint_as_float(rr[0]) + __uint_as_float(rr[1]); }
;     const float rinv = 1.0f / sqrtf(ss * (1.0f / 128.0f) + RMS_EPS);
.LBB0_405:
	s_and_b64 vcc, exec, s[4:5]
	s_cbranch_vccz .LBB0_437
	s_cmp_lg_u32 s100, 0
	s_cbranch_scc1 .Lorig_entry
	v_mov_b32_e32 v147, v0
	s_mul_i32 s2, s71, 0x1800
	s_waitcnt vmcnt(0)
	v_and_b32_e32 v3, 0x60, v147
	v_lshlrev_b32_e32 v5, 3, v147
	v_and_b32_e32 v176, 15, v147
	v_lshrrev_b32_e32 v2, 2, v147
	v_and_or_b32 v3, v5, 24, v3
	v_and_b32_e32 v4, 16, v147
	v_xor_b32_e32 v3, v3, v4
	v_ashrrev_i32_e32 v5, 4, v147
	v_bfe_u32 v146, v147, 2, 2
	v_and_b32_e32 v148, 4, v2
	v_bitop3_b32 v6, v5, v176, 15 bitop3:0x6c
	v_lshlrev_b32_e32 v149, 8, v5
	v_and_b32_e32 v154, 0xfffff0, v5
	v_or_b32_e32 v2, v148, v146
	v_and_b32_e32 v156, 8, v5
	s_mul_hi_u32 s3, s70, 0x1800
	v_lshlrev_b32_e32 v3, 1, v3
	v_or3_b32 v5, v154, v156, v2
	s_add_i32 s3, s3, s2
	s_mul_i32 s2, s70, 0x1800
	v_lshl_or_b32 v30, v5, 8, v3
	v_add_u32_e32 v5, 0x200, v147
	s_add_u32 s2, s22, s2
	v_ashrrev_i32_e32 v5, 4, v5
	s_addc_u32 s3, s88, s3
	s_lshl_b64 s[44:45], s[72:73], 1
	v_lshlrev_b32_e32 v150, 4, v6
	v_bitop3_b32 v6, v5, v176, 15 bitop3:0x6c
	v_lshlrev_b32_e32 v151, 8, v5
	v_and_b32_e32 v153, 0xfffff0, v5
	s_add_u32 s2, s2, s44
	v_ashrrev_i32_e32 v179, 6, v147
	v_and_b32_e32 v155, 8, v5
	s_addc_u32 s3, s3, s45
	v_and_b32_e32 v177, 31, v147
	v_lshlrev_b32_e32 v164, 5, v179
	v_or3_b32 v2, v153, v155, v2
	v_or_b32_e32 v4, v164, v177
	v_lshl_or_b32 v34, v2, 8, v3
	v_mov_b64_e32 v[2:3], s[2:3]
	s_movk_i32 s2, 0x1800
	v_mad_i64_i32 v[2:3], s[2:3], v4, s2, v[2:3]
	v_readfirstlane_b32 s2, v179
	s_lshl_b32 s2, s2, 10
	s_add_i32 s96, s2, 0
	v_or_b32_e32 v162, v150, v149
	s_add_i32 s2, s96, 0x4000
	s_mov_b32 m0, s96
	v_lshlrev_b32_e32 v152, 4, v6
	global_load_lds_dwordx4 v162, s[38:39]
	s_mov_b32 m0, s2
	v_or_b32_e32 v32, v152, v151
	global_load_lds_dwordx4 v30, s[40:41]
	s_add_i32 m0, s96, 0x2000
	v_bfe_u32 v178, v147, 5, 1
	global_load_lds_dwordx4 v32, s[38:39]
	s_add_i32 m0, s96, 0x6000
	s_add_u32 s2, s38, 0x4000
	s_addc_u32 s3, s39, 0
	s_add_u32 s4, s40, 0x4000
	global_load_lds_dwordx4 v34, s[40:41]
	s_addc_u32 s5, s41, 0
	s_add_i32 m0, s96, 0x8000
	s_add_i32 s6, s96, 0xc000
	global_load_lds_dwordx4 v162, s[2:3]
	s_mov_b32 m0, s6
	v_lshlrev_b32_e32 v166, 4, v178
	global_load_lds_dwordx4 v30, s[4:5]
	s_add_i32 m0, s96, 0xa000
	v_mov_b32_e32 v167, v163
	global_load_lds_dwordx4 v32, s[2:3]
	s_add_i32 m0, s96, 0xe000
	v_lshl_add_u64 v[2:3], v[2:3], 0, v[166:167]
	global_load_lds_dwordx4 v34, s[4:5]
	global_load_dwordx4 v[102:105], v[2:3], off
	global_load_dwordx4 v[110:113], v[2:3], off offset:32
	global_load_dwordx4 v[98:101], v[2:3], off offset:64
	global_load_dwordx4 v[106:109], v[2:3], off offset:96
	global_load_dwordx4 v[118:121], v[2:3], off offset:128
	global_load_dwordx4 v[126:129], v[2:3], off offset:160
	global_load_dwordx4 v[114:117], v[2:3], off offset:192
	global_load_dwordx4 v[122:125], v[2:3], off offset:224
	s_cmp_lt_i32 s68, 0
	s_cbranch_scc1 .LBB0_408
	v_lshl_or_b32 v3, s68, 8, v177
	v_lshlrev_b32_e32 v2, 3, v178
	v_add_u32_e32 v26, v3, v164
	v_lshlrev_b32_e32 v44, 2, v2
	v_ashrrev_i32_e32 v2, 1, v26
	v_and_b32_e32 v2, 0xffffffe0, v2
	v_ashrrev_i32_e32 v3, 31, v2
	v_mov_b32_e32 v45, v163
	v_lshl_add_u64 v[2:3], v[2:3], 2, s[16:17]
	v_lshl_add_u64 v[76:77], v[2:3], 0, v[44:45]
	s_mov_b64 s[2:3], 0x4000
	v_lshl_add_u64 v[6:7], v[76:77], 0, s[2:3]
	s_waitcnt lgkmcnt(0)
	global_load_dwordx4 v[130:133], v44, s[14:15] offset:16
	global_load_dwordx4 v[14:17], v44, s[14:15] offset:144
	global_load_dwordx4 v[2:5], v[76:77], off offset:16
	s_nop 0
	global_load_dwordx4 v[6:9], v[6:7], off offset:16
	s_nop 0
	global_load_dwordx4 v[22:25], v44, s[14:15]
	global_load_dwordx4 v[18:21], v44, s[14:15] offset:128
	s_waitcnt vmcnt(0)
	v_lshlrev_b32_e32 v38, 16, v129
	v_and_b32_e32 v36, 0xffff0000, v129
	v_lshlrev_b32_e32 v129, 16, v102
	v_lshlrev_b32_e32 v39, 16, v125
	v_and_b32_e32 v37, 0xffff0000, v125
	v_lshlrev_b32_e32 v49, 16, v123
	v_lshlrev_b32_e32 v48, 16, v127
	v_and_b32_e32 v47, 0xffff0000, v123
	v_and_b32_e32 v46, 0xffff0000, v127
	v_lshlrev_b32_e32 v123, 16, v99
	v_and_b32_e32 v127, 0xffff0000, v99
	v_and_b32_e32 v99, 0xffff0000, v102
	v_lshlrev_b32_e32 v53, 16, v122
	v_and_b32_e32 v51, 0xffff0000, v122
	v_lshlrev_b32_e32 v122, 16, v103
	v_lshlrev_b32_e32 v52, 16, v126
	v_and_b32_e32 v50, 0xffff0000, v126
	v_and_b32_e32 v126, 0xffff0000, v103
	v_lshlrev_b32_e32 v90, 16, v111
	v_and_b32_e32 v88, 0xffff0000, v111
	v_lshlrev_b32_e32 v92, 16, v110
	v_and_b32_e32 v94, 0xffff0000, v110
	v_lshlrev_b32_e32 v111, 16, v100
	v_lshlrev_b32_e32 v110, 16, v104
	v_lshlrev_b32_e32 v65, 16, v116
	v_and_b32_e32 v63, 0xffff0000, v116
	v_lshlrev_b32_e32 v73, 16, v114
	v_and_b32_e32 v71, 0xffff0000, v114
	v_lshlrev_b32_e32 v114, 16, v105
	v_and_b32_e32 v116, 0xffff0000, v105
	v_and_b32_e32 v105, 0xffff0000, v100
	v_and_b32_e32 v104, 0xffff0000, v104
	v_lshlrev_b32_e32 v69, 16, v115
	v_and_b32_e32 v67, 0xffff0000, v115
	v_lshlrev_b32_e32 v115, 16, v101
	v_lshlrev_b32_e32 v61, 16, v117
	v_and_b32_e32 v55, 0xffff0000, v117
	v_and_b32_e32 v117, 0xffff0000, v101
	v_lshlrev_b32_e32 v93, 16, v106
	v_and_b32_e32 v95, 0xffff0000, v106
	v_lshlrev_b32_e32 v91, 16, v107
	v_and_b32_e32 v89, 0xffff0000, v107
	v_lshlrev_b32_e32 v87, 16, v108
	v_lshlrev_b32_e32 v86, 16, v112
	v_and_b32_e32 v85, 0xffff0000, v108
	v_and_b32_e32 v84, 0xffff0000, v112
	v_lshlrev_b32_e32 v83, 16, v109
	v_lshlrev_b32_e32 v82, 16, v113
	v_and_b32_e32 v81, 0xffff0000, v109
	v_and_b32_e32 v80, 0xffff0000, v113
	v_lshlrev_b32_e32 v42, 16, v128
	v_and_b32_e32 v40, 0xffff0000, v128
	v_lshlrev_b32_e32 v128, 16, v98
	v_and_b32_e32 v98, 0xffff0000, v98
	s_movk_i32 s4, 0x4000
	v_lshlrev_b32_e32 v26, 7, v26
	v_add_co_u32_e32 v78, vcc, s4, v76
; __device__ __forceinline__ void attn_dma_body(const bf16_t* __restrict__ Qb, int ldq, int tpos0, const float* __restrict__ rope, const float* __restrict__ qgain, ...
;     ...
;   if (tpos0 >= 0) {
;     float ss = 0.f;
; #pragma unroll
;     for (int d0 = 0; d0 < 8; ++d0)
; #pragma unroll
;       for (int i = 0; i < 8; ++i) { const float x = bf2f((unsigned)(unsigned short)qr[d0][i]); ss += x * x; }
;     { auto rr = __builtin_amdgcn_permlane32_swap(__float_as_uint(ss), __float_as_uint(ss), false, false); ss = __uint_as_float(rr[0]) + __uint_as_float(rr[1]); }
;     const float rinv = 1.0f / sqrtf(ss * (1.0f / 128.0f) + RMS_EPS);
;     const int t = tpos0 + wid * QBLK + r32;
; #pragma unroll
;     for (int ax = 0; ax < 2; ++ax) { const int pos = ax ? (t & 63) : (t >> 6);
; #pragma unroll
;       for (int q = 0; q < 2; ++q) { const int dl = 4 * ax + q, dh = dl + 2, p0 = q * 16 + 8 * hi;
;         const float* cp_ = rope + pos * 32 + p0; const float* gl = qgain + dl * 16 + 8 * hi; const float* gh = qgain + dh * 16 + 8 * hi;
;         float cs[8], sn[8], lo[8], hv[8];
; #pragma unroll
;         for (int i = 0; i < 8; ++i) { cs[i] = cp_[i]; sn[i] = cp_[4096 + i];
;           lo[i] = bf2f((unsigned)(unsigned short)qr[dl][i]) * rinv * gl[i]; hv[i] = bf2f((unsigned)(unsigned short)qr[dh][i]) * rinv * gh[i]; }
	v_mov_b32_e32 v27, v163
	v_and_b32_e32 v26, 0x1f80, v26
	v_addc_co_u32_e32 v79, vcc, 0, v77, vcc
	v_lshl_add_u64 v[26:27], s[16:17], 0, v[26:27]
	global_load_dwordx4 v[10:13], v[78:79], off
	v_lshl_add_u64 v[58:59], v[26:27], 0, v[44:45]
	global_load_dwordx4 v[26:29], v[76:77], off
	v_lshlrev_b32_e32 v72, 16, v118
	v_and_b32_e32 v70, 0xffff0000, v118
	v_lshlrev_b32_e32 v68, 16, v119
	v_and_b32_e32 v66, 0xffff0000, v119
	v_lshlrev_b32_e32 v64, 16, v120
	v_and_b32_e32 v62, 0xffff0000, v120
	v_lshlrev_b32_e32 v60, 16, v121
	v_and_b32_e32 v54, 0xffff0000, v121
	v_lshlrev_b32_e32 v43, 16, v124
	v_and_b32_e32 v41, 0xffff0000, v124
	v_mov_b32_e32 v134, v37
	v_mov_b32_e32 v135, v39
	v_lshl_add_u64 v[74:75], v[58:59], 0, s[2:3]
	v_mov_b32_e32 v125, v20
	v_mul_f32_e32 v20, v129, v129
	v_fmac_f32_e32 v20, v99, v99
	v_pk_fma_f32 v[102:103], v[122:123], v[122:123], v[20:21] op_sel_hi:[1,1,0]
	v_mul_f32_e32 v20, v123, v123
	v_pk_fma_f32 v[102:103], v[126:127], v[126:127], v[102:103]
	s_mov_b32 s2, 0xf800000
	v_pk_fma_f32 v[102:103], v[110:111], v[110:111], v[102:103]
	v_mov_b32_e32 v124, v24
	v_pk_fma_f32 v[102:103], v[104:105], v[104:105], v[102:103]
	v_mov_b32_e32 v120, v130
	v_pk_fma_f32 v[102:103], v[114:115], v[114:115], v[102:103]
	v_mov_b32_e32 v121, v14
	v_pk_fma_f32 v[102:103], v[116:117], v[116:117], v[102:103]
	v_mov_b32_e32 v14, v131
	v_pk_fma_f32 v[102:103], v[92:93], v[92:93], v[102:103]
	v_mov_b32_e32 v118, v132
	v_pk_fma_f32 v[102:103], v[94:95], v[94:95], v[102:103]
	v_mov_b32_e32 v119, v16
	v_pk_fma_f32 v[102:103], v[90:91], v[90:91], v[102:103]
	v_mov_b32_e32 v16, v133
	v_pk_fma_f32 v[102:103], v[88:89], v[88:89], v[102:103]
	v_mov_b32_e32 v106, v6
	v_pk_fma_f32 v[102:103], v[86:87], v[86:87], v[102:103]
	v_mov_b32_e32 v107, v2
	v_pk_fma_f32 v[102:103], v[84:85], v[84:85], v[102:103]
	v_lshl_add_u64 v[96:97], v[76:77], 0, s[24:25]
	v_pk_fma_f32 v[102:103], v[82:83], v[82:83], v[102:103]
	v_mov_b32_e32 v112, v8
	v_pk_fma_f32 v[102:103], v[80:81], v[80:81], v[102:103]
	v_mov_b32_e32 v113, v4
	v_pk_fma_f32 v[102:103], v[128:129], v[128:129], v[102:103]
	v_mov_b32_e32 v108, v9
	v_pk_fma_f32 v[102:103], v[98:99], v[98:99], v[102:103]
	v_mov_b32_e32 v109, v5
	v_pk_add_f32 v[102:103], v[20:21], v[102:103] op_sel_hi:[0,1]
	v_mul_f32_e32 v20, v127, v127
	v_pk_add_f32 v[102:103], v[20:21], v[102:103] op_sel_hi:[0,1]
	v_mul_f32_e32 v20, v111, v111
	v_pk_add_f32 v[102:103], v[20:21], v[102:103] op_sel_hi:[0,1]
	v_mul_f32_e32 v20, v105, v105
	v_pk_add_f32 v[102:103], v[20:21], v[102:103] op_sel_hi:[0,1]
	v_mul_f32_e32 v20, v115, v115
	v_pk_add_f32 v[102:103], v[20:21], v[102:103] op_sel_hi:[0,1]
	v_mul_f32_e32 v20, v117, v117
	v_pk_add_f32 v[102:103], v[20:21], v[102:103] op_sel_hi:[0,1]
	v_mul_f32_e32 v20, v93, v93
	v_pk_add_f32 v[102:103], v[20:21], v[102:103] op_sel_hi:[0,1]
	v_mul_f32_e32 v20, v95, v95
	v_pk_add_f32 v[102:103], v[20:21], v[102:103] op_sel_hi:[0,1]
	v_mul_f32_e32 v20, v91, v91
	v_pk_add_f32 v[102:103], v[20:21], v[102:103] op_sel_hi:[0,1]
	v_mul_f32_e32 v20, v89, v89
	v_pk_add_f32 v[102:103], v[20:21], v[102:103] op_sel_hi:[0,1]
	v_mul_f32_e32 v20, v87, v87
	v_pk_add_f32 v[102:103], v[20:21], v[102:103] op_sel_hi:[0,1]
	v_mul_f32_e32 v20, v85, v85
	v_pk_add_f32 v[102:103], v[20:21], v[102:103] op_sel_hi:[0,1]
	v_mul_f32_e32 v20, v83, v83
	v_pk_add_f32 v[102:103], v[20:21], v[102:103] op_sel_hi:[0,1]
	v_mul_f32_e32 v20, v81, v81
	v_pk_add_f32 v[102:103], v[20:21], v[102:103] op_sel_hi:[0,1]
	v_pk_fma_f32 v[102:103], v[72:73], v[72:73], v[102:103]
	v_mul_f32_e32 v20, v73, v73
	v_pk_fma_f32 v[102:103], v[70:71], v[70:71], v[102:103]
	s_waitcnt vmcnt(1)
	v_mov_b32_e32 v100, v12
	v_pk_fma_f32 v[102:103], v[68:69], v[68:69], v[102:103]
	s_waitcnt vmcnt(0)
	v_mov_b32_e32 v101, v28
	v_pk_fma_f32 v[102:103], v[66:67], v[66:67], v[102:103]
	v_lshl_add_u64 v[56:57], v[58:59], 0, s[24:25]
	v_pk_fma_f32 v[102:103], v[64:65], v[64:65], v[102:103]
	s_nop 0
	v_pk_fma_f32 v[102:103], v[62:63], v[62:63], v[102:103]
	s_nop 0
	v_pk_fma_f32 v[102:103], v[60:61], v[60:61], v[102:103]
	s_nop 0
	v_pk_fma_f32 v[102:103], v[54:55], v[54:55], v[102:103]
	s_nop 0
	v_pk_fma_f32 v[102:103], v[52:53], v[52:53], v[102:103]
	s_nop 0
	v_pk_fma_f32 v[102:103], v[50:51], v[50:51], v[102:103]
	s_nop 0
	v_pk_fma_f32 v[102:103], v[48:49], v[48:49], v[102:103]
	s_nop 0
	v_pk_fma_f32 v[102:103], v[46:47], v[46:47], v[102:103]
	s_nop 0
	v_pk_fma_f32 v[102:103], v[42:43], v[42:43], v[102:103]
	s_nop 0
	v_pk_fma_f32 v[102:103], v[40:41], v[40:41], v[102:103]
	s_nop 0
	v_pk_fma_f32 v[102:103], v[38:39], v[38:39], v[102:103]
	s_nop 0
	v_pk_fma_f32 v[102:103], v[36:37], v[36:37], v[102:103]
	s_nop 0
	v_pk_add_f32 v[102:103], v[20:21], v[102:103] op_sel_hi:[0,1]
	v_mul_f32_e32 v20, v71, v71
	v_pk_add_f32 v[102:103], v[20:21], v[102:103] op_sel_hi:[0,1]
	v_mul_f32_e32 v20, v69, v69
	v_pk_add_f32 v[102:103], v[20:21], v[102:103] op_sel_hi:[0,1]
	v_mul_f32_e32 v20, v67, v67
	v_pk_add_f32 v[102:103], v[20:21], v[102:103] op_sel_hi:[0,1]
	v_mul_f32_e32 v20, v65, v65
	v_pk_add_f32 v[102:103], v[20:21], v[102:103] op_sel_hi:[0,1]
	v_mul_f32_e32 v20, v63, v63
	v_pk_add_f32 v[102:103], v[20:21], v[102:103] op_sel_hi:[0,1]
	v_mul_f32_e32 v20, v61, v61
	v_pk_add_f32 v[102:103], v[20:21], v[102:103] op_sel_hi:[0,1]
	v_mul_f32_e32 v20, v55, v55
	v_pk_add_f32 v[102:103], v[20:21], v[102:103] op_sel_hi:[0,1]
	v_mul_f32_e32 v20, v53, v53
	v_pk_add_f32 v[102:103], v[20:21], v[102:103] op_sel_hi:[0,1]
	v_mul_f32_e32 v20, v51, v51
	v_pk_add_f32 v[102:103], v[20:21], v[102:103] op_sel_hi:[0,1]
	v_mul_f32_e32 v20, v49, v49
	v_pk_add_f32 v[102:103], v[20:21], v[102:103] op_sel_hi:[0,1]
; __device__ __forceinline__ unsigned pk2(float lo, float hi) { unsigned r; asm("v_cvt_pk_bf16_f32 %0, %1, %2" : "=v"(r) : "v"(lo), "v"(hi)); return r; }
; __device__ __forceinline__ void attn_dma_body(const bf16_t* __restrict__ Qb, int ldq, int tpos0, const float* __restrict__ rope, const float* __restrict__ qgain, ...
;     ...
;     { auto rr = __builtin_amdgcn_permlane32_swap(__float_as_uint(ss), __float_as_uint(ss), false, false); ss = __uint_as_float(rr[0]) + __uint_as_float(rr[1]); }
;     const float rinv = 1.0f / sqrtf(ss * (1.0f / 128.0f) + RMS_EPS);
;     const int t = tpos0 + wid * QBLK + r32;
; #pragma unroll
;     for (int ax = 0; ax < 2; ++ax) { const int pos = ax ? (t & 63) : (t >> 6);
; #pragma unroll
;       for (int q = 0; q < 2; ++q) { const int dl = 4 * ax + q, dh = dl + 2, p0 = q * 16 + 8 * hi;
;         const float* cp_ = rope + pos * 32 + p0; const float* gl = qgain + dl * 16 + 8 * hi; const float* gh = qgain + dh * 16 + 8 * hi;
;         float cs[8], sn[8], lo[8], hv[8];
; #pragma unroll
;         for (int i = 0; i < 8; ++i) { cs[i] = cp_[i]; sn[i] = cp_[4096 + i];
;           lo[i] = bf2f((unsigned)(unsigned short)qr[dl][i]) * rinv * gl[i]; hv[i] = bf2f((unsigned)(unsigned short)qr[dh][i]) * rinv * gh[i]; }
;         u32x4 wl, wh;
; #pragma unroll
;         for (int i = 0; i < 4; ++i) { const float l0 = lo[2 * i] * cs[2 * i] - hv[2 * i] * sn[2 * i], l1 = lo[2 * i + 1] * cs[2 * i + 1] - hv[2 * i + 1] * sn[2 * i + 1];
;           const float h0 = hv[2 * i] * cs[2 * i] + lo[2 * i] * sn[2 * i], h1 = hv[2 * i + 1] * cs[2 * i + 1] + lo[2 * i + 1] * sn[2 * i + 1];
;           wl[i] = pk2(l0, l1); wh[i] = pk2(h0, h1); }
;         qr[dl] = *reinterpret_cast<bf16x8*>(&wl); qr[dh] = *reinterpret_cast<bf16x8*>(&wh); } } }
	v_mul_f32_e32 v20, v47, v47
	v_pk_add_f32 v[102:103], v[20:21], v[102:103] op_sel_hi:[0,1]
	v_mul_f32_e32 v20, v43, v43
	v_pk_add_f32 v[102:103], v[20:21], v[102:103] op_sel_hi:[0,1]
	v_mul_f32_e32 v20, v41, v41
	v_pk_add_f32 v[102:103], v[20:21], v[102:103] op_sel_hi:[0,1]
	v_mul_f32_e32 v20, v39, v39
	v_pk_add_f32 v[102:103], v[20:21], v[102:103] op_sel_hi:[0,1]
	v_pk_fma_f32 v[102:103], v[134:135], v[134:135], v[102:103]
	global_load_dwordx4 v[130:133], v44, s[14:15] offset:80
	global_load_dwordx4 v[134:137], v44, s[14:15] offset:64
	global_load_dwordx4 v[138:141], v44, s[14:15] offset:208
	global_load_dwordx4 v[142:145], v44, s[14:15] offset:192
	v_mov_b32_e32 v20, v102
	s_nop 1
	v_permlane32_swap_b32_e32 v102, v20
	v_add_f32_e32 v20, v102, v20
	v_fmamk_f32 v20, v20, 0x3c000000, v1
	v_mul_f32_e32 v24, 0x4f800000, v20
	v_cmp_gt_f32_e32 vcc, s2, v20
	v_mov_b32_e32 v102, v26
	v_mov_b32_e32 v103, v10
	v_cndmask_b32_e32 v31, v20, v24, vcc
	v_sqrt_f32_e32 v33, v31
	v_mov_b32_e32 v24, v18
	v_mov_b32_e32 v20, v25
	v_add_u32_e32 v18, -1, v33
	v_fma_f32 v25, -v18, v33, v31
	v_cmp_ge_f32_e64 s[2:3], 0, v25
	v_add_u32_e32 v25, 1, v33
	s_nop 0
	v_cndmask_b32_e64 v18, v33, v18, s[2:3]
	v_fma_f32 v33, -v25, v33, v31
	v_cmp_lt_f32_e64 s[2:3], 0, v33
	s_nop 1
	v_cndmask_b32_e64 v18, v18, v25, s[2:3]
	v_mul_f32_e32 v25, 0x37800000, v18
	v_cndmask_b32_e32 v18, v18, v25, vcc
	v_cmp_class_f32_e32 vcc, v31, v174
	v_mov_b32_e32 v25, v22
	s_nop 0
	v_cndmask_b32_e32 v18, v18, v31, vcc
	v_div_scale_f32 v31, s[2:3], v18, v18, 1.0
	v_rcp_f32_e32 v33, v31
	s_nop 0
	v_fma_f32 v22, -v31, v33, 1.0
	v_fmac_f32_e32 v33, v22, v33
	v_div_scale_f32 v22, vcc, 1.0, v18, 1.0
	v_mul_f32_e32 v35, v22, v33
	v_fma_f32 v45, -v31, v35, v22
	v_fmac_f32_e32 v35, v45, v33
	v_fma_f32 v22, -v31, v35, v22
	v_div_fmas_f32 v22, v22, v33, v35
	v_div_fixup_f32 v18, v22, v18, 1.0
	v_mul_f32_e32 v18, 0x3e0293ee, v18
	v_pk_mul_f32 v[98:99], v[18:19], v[98:99] op_sel_hi:[0,1]
	v_mov_b32_e32 v22, v19
	v_pk_mul_f32 v[98:99], v[98:99], v[22:23]
	v_pk_mul_f32 v[22:23], v[18:19], v[122:123] op_sel_hi:[0,1]
	v_pk_mul_f32 v[122:123], v[22:23], v[124:125]
	v_pk_mul_f32 v[22:23], v[18:19], v[126:127] op_sel_hi:[0,1]
	v_pk_mul_f32 v[124:125], v[22:23], v[20:21]
	v_pk_mul_f32 v[20:21], v[18:19], v[110:111] op_sel_hi:[0,1]
	v_pk_mul_f32 v[110:111], v[20:21], v[120:121]
	v_pk_mul_f32 v[20:21], v[18:19], v[104:105] op_sel_hi:[0,1]
	v_pk_mul_f32 v[104:105], v[20:21], v[14:15]
	v_pk_mul_f32 v[14:15], v[18:19], v[114:115] op_sel_hi:[0,1]
	v_pk_mul_f32 v[128:129], v[18:19], v[128:129] op_sel_hi:[0,1]
	v_pk_mul_f32 v[114:115], v[14:15], v[118:119]
	v_pk_mul_f32 v[14:15], v[18:19], v[116:117] op_sel_hi:[0,1]
	v_pk_mul_f32 v[24:25], v[24:25], v[128:129]
	v_pk_mul_f32 v[116:117], v[14:15], v[16:17]
	v_mov_b32_e32 v14, v10
	v_mov_b32_e32 v15, v26
	v_pk_mul_f32 v[14:15], v[14:15], v[24:25]
	v_mov_b32_e32 v26, v11
	v_sub_f32_e32 v19, v15, v14
	v_pk_mul_f32 v[14:15], v[26:27], v[98:99]
	v_mov_b32_e32 v10, v27
	v_sub_f32_e32 v31, v15, v14
	v_pk_mul_f32 v[14:15], v[102:103], v[24:25]
	v_pk_mul_f32 v[10:11], v[10:11], v[98:99]
	v_add_f32_e32 v33, v14, v15
	global_load_dwordx4 v[14:17], v[76:77], off offset:80
	global_load_dwordx4 v[20:23], v[76:77], off offset:64
	global_load_dwordx4 v[24:27], v[78:79], off offset:64
	v_add_f32_e32 v10, v10, v11
	v_cvt_pk_bf16_f32 v98, v33, v10
	v_mov_b32_e32 v10, v28
	v_mov_b32_e32 v11, v12
	v_pk_mul_f32 v[10:11], v[10:11], v[122:123]
	v_mov_b32_e32 v12, v29
	v_cvt_pk_bf16_f32 v102, v19, v31
	v_sub_f32_e32 v19, v10, v11
	v_pk_mul_f32 v[10:11], v[12:13], v[124:125]
	v_mov_b32_e32 v28, v13
	v_sub_f32_e32 v12, v10, v11
	v_pk_mul_f32 v[10:11], v[100:101], v[122:123]
	v_cvt_pk_bf16_f32 v103, v19, v12
	s_waitcnt vmcnt(3)
	v_mov_b32_e32 v13, v144
	v_add_f32_e32 v31, v10, v11
	v_pk_mul_f32 v[10:11], v[28:29], v[124:125]
	v_mov_b32_e32 v144, v137
	v_add_f32_e32 v10, v10, v11
	v_cvt_pk_bf16_f32 v99, v31, v10
	v_mov_b32_e32 v10, v2
	v_mov_b32_e32 v11, v6
	v_pk_mul_f32 v[10:11], v[10:11], v[110:111]
	v_mov_b32_e32 v6, v3
	v_mov_b32_e32 v2, v7
	v_sub_f32_e32 v12, v10, v11
	v_pk_mul_f32 v[10:11], v[6:7], v[104:105]
	v_pk_mul_f32 v[2:3], v[2:3], v[104:105]
	v_sub_f32_e32 v6, v10, v11
	v_pk_mul_f32 v[10:11], v[106:107], v[110:111]
	v_add_f32_e32 v2, v2, v3
	v_add_f32_e32 v10, v10, v11
	v_cvt_pk_bf16_f32 v100, v10, v2
	v_mov_b32_e32 v2, v4
	v_mov_b32_e32 v3, v8
	v_pk_mul_f32 v[2:3], v[2:3], v[114:115]
	v_mov_b32_e32 v8, v5
	v_cvt_pk_bf16_f32 v104, v12, v6
	v_sub_f32_e32 v4, v2, v3
	v_pk_mul_f32 v[2:3], v[8:9], v[116:117]
	global_load_dwordx4 v[6:9], v[96:97], off offset:16
	v_sub_f32_e32 v5, v2, v3
	v_pk_mul_f32 v[2:3], v[112:113], v[114:115]
	v_mov_b32_e32 v12, v136
	v_add_f32_e32 v10, v2, v3
	v_pk_mul_f32 v[2:3], v[108:109], v[116:117]
	v_cvt_pk_bf16_f32 v105, v4, v5
	v_mov_b32_e32 v4, v134
	v_add_f32_e32 v2, v2, v3
	v_cvt_pk_bf16_f32 v101, v10, v2
	v_pk_mul_f32 v[10:11], v[18:19], v[90:91] op_sel_hi:[0,1]
	v_pk_mul_f32 v[28:29], v[10:11], v[12:13]
	v_pk_mul_f32 v[10:11], v[18:19], v[88:89] op_sel_hi:[0,1]
	v_pk_mul_f32 v[96:97], v[10:11], v[144:145]
	v_pk_mul_f32 v[10:11], v[18:19], v[86:87] op_sel_hi:[0,1]
	v_mov_b32_e32 v12, v130
	v_mov_b32_e32 v13, v138
	v_pk_mul_f32 v[2:3], v[18:19], v[92:93] op_sel_hi:[0,1]
	v_mov_b32_e32 v5, v142
	v_pk_mul_f32 v[108:109], v[10:11], v[12:13]
	v_mov_b32_e32 v13, v140
	v_pk_mul_f32 v[88:89], v[18:19], v[80:81] op_sel_hi:[0,1]
	v_mov_b32_e32 v140, v133
	v_pk_mul_f32 v[2:3], v[2:3], v[4:5]
	v_pk_mul_f32 v[116:117], v[88:89], v[140:141]
	v_pk_mul_f32 v[4:5], v[18:19], v[94:95] op_sel_hi:[0,1]
	v_mov_b32_e32 v142, v135
	v_pk_mul_f32 v[10:11], v[18:19], v[84:85] op_sel_hi:[0,1]
	v_mov_b32_e32 v138, v131
	v_pk_mul_f32 v[4:5], v[4:5], v[142:143]
	v_pk_mul_f32 v[112:113], v[10:11], v[138:139]
	v_pk_mul_f32 v[10:11], v[18:19], v[82:83] op_sel_hi:[0,1]
	v_mov_b32_e32 v12, v132
	v_pk_mul_f32 v[114:115], v[10:11], v[12:13]
	global_load_dwordx4 v[10:13], v44, s[14:15] offset:272
	global_load_dwordx4 v[76:79], v44, s[14:15] offset:256
	global_load_dwordx4 v[80:83], v44, s[14:15] offset:400
	global_load_dwordx4 v[84:87], v44, s[14:15] offset:384
	v_add_co_u32_e32 v118, vcc, s4, v58
	s_waitcnt vmcnt(6)
; __device__ __forceinline__ unsigned pk2(float lo, float hi) { unsigned r; asm("v_cvt_pk_bf16_f32 %0, %1, %2" : "=v"(r) : "v"(lo), "v"(hi)); return r; }
; __device__ __forceinline__ void attn_dma_body(const bf16_t* __restrict__ Qb, int ldq, int tpos0, const float* __restrict__ rope, const float* __restrict__ qgain, ...
;     ...
;     for (int ax = 0; ax < 2; ++ax) { const int pos = ax ? (t & 63) : (t >> 6);
; #pragma unroll
;       for (int q = 0; q < 2; ++q) { const int dl = 4 * ax + q, dh = dl + 2, p0 = q * 16 + 8 * hi;
;         const float* cp_ = rope + pos * 32 + p0; const float* gl = qgain + dl * 16 + 8 * hi; const float* gh = qgain + dh * 16 + 8 * hi;
;         float cs[8], sn[8], lo[8], hv[8];
; #pragma unroll
;         for (int i = 0; i < 8; ++i) { cs[i] = cp_[i]; sn[i] = cp_[4096 + i];
;           lo[i] = bf2f((unsigned)(unsigned short)qr[dl][i]) * rinv * gl[i]; hv[i] = bf2f((unsigned)(unsigned short)qr[dh][i]) * rinv * gh[i]; }
;         u32x4 wl, wh;
; #pragma unroll
;         for (int i = 0; i < 4; ++i) { const float l0 = lo[2 * i] * cs[2 * i] - hv[2 * i] * sn[2 * i], l1 = lo[2 * i + 1] * cs[2 * i + 1] - hv[2 * i + 1] * sn[2 * i + 1];
;           const float h0 = hv[2 * i] * cs[2 * i] + lo[2 * i] * sn[2 * i], h1 = hv[2 * i + 1] * cs[2 * i + 1] + lo[2 * i + 1] * sn[2 * i + 1];
;           wl[i] = pk2(l0, l1); wh[i] = pk2(h0, h1); }
;         qr[dl] = *reinterpret_cast<bf16x8*>(&wl); qr[dh] = *reinterpret_cast<bf16x8*>(&wh); } } }
	v_mov_b32_e32 v88, v20
	s_waitcnt vmcnt(5)
	v_mov_b32_e32 v89, v24
	v_pk_mul_f32 v[88:89], v[88:89], v[2:3]
	v_addc_co_u32_e32 v119, vcc, 0, v59, vcc
	v_sub_f32_e32 v19, v88, v89
	v_mov_b32_e32 v88, v21
	v_mov_b32_e32 v89, v25
	v_pk_mul_f32 v[88:89], v[88:89], v[4:5]
	s_nop 0
	v_sub_f32_e32 v31, v88, v89
	v_mov_b32_e32 v88, v24
	v_mov_b32_e32 v89, v20
	v_pk_mul_f32 v[2:3], v[88:89], v[2:3]
	v_mov_b32_e32 v20, v25
	v_add_f32_e32 v24, v2, v3
	v_pk_mul_f32 v[2:3], v[20:21], v[4:5]
	v_cvt_pk_bf16_f32 v110, v19, v31
	s_nop 0
	v_add_f32_e32 v2, v2, v3
	v_cvt_pk_bf16_f32 v106, v24, v2
	v_mov_b32_e32 v2, v22
	v_mov_b32_e32 v3, v26
	v_pk_mul_f32 v[2:3], v[2:3], v[28:29]
	s_nop 0
	v_sub_f32_e32 v19, v2, v3
	v_mov_b32_e32 v2, v23
	v_mov_b32_e32 v3, v27
	v_pk_mul_f32 v[20:21], v[2:3], v[96:97]
	global_load_dwordx4 v[2:5], v[58:59], off offset:16
	global_load_dwordx4 v[88:91], v[58:59], off
	global_load_dwordx4 v[92:95], v[118:119], off
	v_sub_f32_e32 v24, v20, v21
	v_mov_b32_e32 v20, v26
	v_mov_b32_e32 v21, v22
	v_pk_mul_f32 v[20:21], v[20:21], v[28:29]
	v_mov_b32_e32 v22, v27
	v_add_f32_e32 v25, v20, v21
	v_pk_mul_f32 v[20:21], v[22:23], v[96:97]
	v_cvt_pk_bf16_f32 v111, v19, v24
	s_nop 0
	v_add_f32_e32 v20, v20, v21
	v_cvt_pk_bf16_f32 v107, v25, v20
	v_mov_b32_e32 v20, v14
	s_waitcnt vmcnt(7)
	v_mov_b32_e32 v21, v6
	v_pk_mul_f32 v[20:21], v[20:21], v[108:109]
	s_nop 0
	v_sub_f32_e32 v19, v20, v21
	v_mov_b32_e32 v20, v15
	v_mov_b32_e32 v21, v7
	v_pk_mul_f32 v[20:21], v[20:21], v[112:113]
	s_nop 0
	v_sub_f32_e32 v22, v20, v21
	v_mov_b32_e32 v21, v14
	v_mov_b32_e32 v14, v7
	v_mov_b32_e32 v20, v6
	v_pk_mul_f32 v[6:7], v[14:15], v[112:113]
	v_pk_mul_f32 v[20:21], v[20:21], v[108:109]
	v_add_f32_e32 v6, v6, v7
	v_add_f32_e32 v20, v20, v21
	v_cvt_pk_bf16_f32 v108, v20, v6
	v_mov_b32_e32 v6, v16
	v_mov_b32_e32 v7, v8
	v_cvt_pk_bf16_f32 v112, v19, v22
	v_pk_mul_f32 v[6:7], v[6:7], v[114:115]
	global_load_dwordx4 v[20:23], v[74:75], off offset:16
	v_sub_f32_e32 v14, v6, v7
	v_mov_b32_e32 v6, v17
	v_mov_b32_e32 v7, v9
	v_pk_mul_f32 v[6:7], v[6:7], v[116:117]
	s_nop 0
	v_sub_f32_e32 v15, v6, v7
	v_mov_b32_e32 v6, v8
	v_mov_b32_e32 v7, v16
	v_pk_mul_f32 v[6:7], v[6:7], v[114:115]
	v_mov_b32_e32 v16, v9
	v_add_f32_e32 v8, v6, v7
	v_pk_mul_f32 v[6:7], v[16:17], v[116:117]
	s_waitcnt vmcnt(4)
	v_mov_b32_e32 v9, v84
	v_add_f32_e32 v6, v6, v7
	v_cvt_pk_bf16_f32 v109, v8, v6
	v_pk_mul_f32 v[6:7], v[18:19], v[72:73] op_sel_hi:[0,1]
	v_mov_b32_e32 v8, v76
	v_pk_mul_f32 v[28:29], v[6:7], v[8:9]
	v_pk_mul_f32 v[6:7], v[18:19], v[70:71] op_sel_hi:[0,1]
	v_mov_b32_e32 v84, v77
	v_pk_mul_f32 v[70:71], v[6:7], v[84:85]
	v_pk_mul_f32 v[6:7], v[18:19], v[68:69] op_sel_hi:[0,1]
	v_mov_b32_e32 v8, v78
	v_mov_b32_e32 v9, v86
	v_pk_mul_f32 v[72:73], v[6:7], v[8:9]
	v_pk_mul_f32 v[6:7], v[18:19], v[66:67] op_sel_hi:[0,1]
	v_mov_b32_e32 v86, v79
	v_pk_mul_f32 v[74:75], v[6:7], v[86:87]
	v_pk_mul_f32 v[6:7], v[18:19], v[64:65] op_sel_hi:[0,1]
	v_mov_b32_e32 v8, v10
	v_mov_b32_e32 v9, v80
	v_pk_mul_f32 v[76:77], v[6:7], v[8:9]
	v_pk_mul_f32 v[6:7], v[18:19], v[62:63] op_sel_hi:[0,1]
	v_mov_b32_e32 v80, v11
	v_pk_mul_f32 v[10:11], v[18:19], v[60:61] op_sel_hi:[0,1]
	v_mov_b32_e32 v64, v12
	v_mov_b32_e32 v65, v82
	v_cvt_pk_bf16_f32 v113, v14, v15
	v_pk_mul_f32 v[78:79], v[6:7], v[80:81]
	global_load_dwordx4 v[6:9], v44, s[14:15] offset:336
	global_load_dwordx4 v[14:17], v44, s[14:15] offset:320
	global_load_dwordx4 v[24:27], v44, s[14:15] offset:464
	global_load_dwordx4 v[60:63], v44, s[14:15] offset:448
	v_pk_mul_f32 v[44:45], v[10:11], v[64:65]
	v_pk_mul_f32 v[10:11], v[18:19], v[54:55] op_sel_hi:[0,1]
	v_mov_b32_e32 v82, v13
	v_pk_mul_f32 v[80:81], v[10:11], v[82:83]
	s_waitcnt vmcnt(6)
	v_mov_b32_e32 v54, v88
	s_waitcnt vmcnt(5)
	v_mov_b32_e32 v55, v92
	v_pk_mul_f32 v[54:55], v[54:55], v[28:29]
	global_load_dwordx4 v[10:13], v[118:119], off offset:64
	v_sub_f32_e32 v19, v54, v55
	v_mov_b32_e32 v54, v89
	v_mov_b32_e32 v55, v93
	v_pk_mul_f32 v[54:55], v[54:55], v[70:71]
	s_nop 0
	v_sub_f32_e32 v31, v54, v55
	v_mov_b32_e32 v54, v92
	v_mov_b32_e32 v55, v88
	v_pk_mul_f32 v[28:29], v[54:55], v[28:29]
	v_mov_b32_e32 v88, v93
	v_add_f32_e32 v33, v28, v29
	v_pk_mul_f32 v[28:29], v[88:89], v[70:71]
	global_load_dwordx4 v[64:67], v[58:59], off offset:80
	global_load_dwordx4 v[68:71], v[58:59], off offset:64
	v_add_f32_e32 v28, v28, v29
	global_load_dwordx4 v[54:57], v[56:57], off offset:16
	v_cvt_pk_bf16_f32 v114, v33, v28
	v_mov_b32_e32 v28, v90
	v_mov_b32_e32 v29, v94
	v_pk_mul_f32 v[28:29], v[28:29], v[72:73]
	v_cvt_pk_bf16_f32 v118, v19, v31
	s_nop 0
	v_sub_f32_e32 v19, v28, v29
	v_mov_b32_e32 v28, v91
	v_mov_b32_e32 v29, v95
	v_pk_mul_f32 v[28:29], v[28:29], v[74:75]
	s_nop 0
	v_sub_f32_e32 v31, v28, v29
	v_mov_b32_e32 v28, v94
	v_mov_b32_e32 v29, v90
	v_pk_mul_f32 v[28:29], v[28:29], v[72:73]
	v_mov_b32_e32 v90, v95
	v_add_f32_e32 v33, v28, v29
	v_pk_mul_f32 v[28:29], v[90:91], v[74:75]
	v_cvt_pk_bf16_f32 v119, v19, v31
	s_nop 0
	v_add_f32_e32 v28, v28, v29
	v_cvt_pk_bf16_f32 v115, v33, v28
	v_mov_b32_e32 v28, v2
	s_waitcnt vmcnt(8)
	v_mov_b32_e32 v29, v20
	v_pk_mul_f32 v[28:29], v[28:29], v[76:77]
	s_nop 0
	v_sub_f32_e32 v19, v28, v29
	v_mov_b32_e32 v28, v3
	v_mov_b32_e32 v29, v21
	v_pk_mul_f32 v[28:29], v[28:29], v[78:79]
	s_nop 0
	v_sub_f32_e32 v31, v28, v29
	v_mov_b32_e32 v29, v2
	v_mov_b32_e32 v2, v21
	v_mov_b32_e32 v28, v20
	v_pk_mul_f32 v[2:3], v[2:3], v[78:79]
	v_pk_mul_f32 v[28:29], v[28:29], v[76:77]
	v_add_f32_e32 v2, v2, v3
	v_add_f32_e32 v20, v28, v29
	v_cvt_pk_bf16_f32 v116, v20, v2
	v_mov_b32_e32 v2, v4
	v_mov_b32_e32 v3, v22
	v_pk_mul_f32 v[2:3], v[2:3], v[44:45]
	v_cvt_pk_bf16_f32 v120, v19, v31
	s_nop 0
	v_sub_f32_e32 v19, v2, v3
	v_mov_b32_e32 v2, v5
	v_mov_b32_e32 v3, v23
	v_pk_mul_f32 v[2:3], v[2:3], v[80:81]
	s_nop 0
	v_sub_f32_e32 v20, v2, v3
	v_mov_b32_e32 v2, v22
	v_mov_b32_e32 v3, v4
	v_pk_mul_f32 v[2:3], v[2:3], v[44:45]
	v_mov_b32_e32 v4, v23
	v_add_f32_e32 v21, v2, v3
	v_pk_mul_f32 v[2:3], v[4:5], v[80:81]
	v_cvt_pk_bf16_f32 v121, v19, v20
	s_waitcnt vmcnt(6)
; __device__ __forceinline__ unsigned pk2(float lo, float hi) { unsigned r; asm("v_cvt_pk_bf16_f32 %0, %1, %2" : "=v"(r) : "v"(lo), "v"(hi)); return r; }
; __device__ __forceinline__ int v_rd_base(int lane) { return ((lane & 3) << 3) | (((lane >> 2) & 3) << 6) | (((lane >> 4) & 1) << 5) | (((lane >> 5) & 1) << 8); }
; #define ATT_WAIT_BAR() asm volatile("s_waitcnt vmcnt(0) lgkmcnt(0)\n\ts_barrier" ::: "memory")
; __device__ __forceinline__ void attn_dma_body(const bf16_t* __restrict__ Qb, int ldq, int tpos0, const float* __restrict__ rope, const float* __restrict__ qgain, ...
;     ...
;         for (int i = 0; i < 4; ++i) { const float l0 = lo[2 * i] * cs[2 * i] - hv[2 * i] * sn[2 * i], l1 = lo[2 * i + 1] * cs[2 * i + 1] - hv[2 * i + 1] * sn[2 * i + 1];
;           const float h0 = hv[2 * i] * cs[2 * i] + lo[2 * i] * sn[2 * i], h1 = hv[2 * i + 1] * cs[2 * i + 1] + lo[2 * i + 1] * sn[2 * i + 1];
;           wl[i] = pk2(l0, l1); wh[i] = pk2(h0, h1); }
;         qr[dl] = *reinterpret_cast<bf16x8*>(&wl); qr[dh] = *reinterpret_cast<bf16x8*>(&wh); } } }
; #pragma unroll
;   for (int d0 = 0; d0 < 8; ++d0) asm volatile("" : "+v"(qr[d0]));
;   ATT_WAIT_BAR();
;   if (2 < NT) ATT_DMA(2, 2);
;   const int vb0 = (int)(uintptr_t)lds + 16384 + v_rd_base(lane);
;   f32x16 pA0, pA1, pB0, pB1; float mnA, mnB, alA, alB; bf16x8 pa0, pa1, pa2, pa3;
;   qkt(pA0, pA1, (const bf16_t*)lds, qr, r32, hi); partialSM(pA0, pA1, m_reg, mnA, alA);
;   const bool lead = __builtin_amdgcn_readfirstlane(wid) < 4;
	v_mov_b32_e32 v4, v14
	v_add_f32_e32 v2, v2, v3
	v_cvt_pk_bf16_f32 v117, v21, v2
	s_waitcnt vmcnt(4)
	v_mov_b32_e32 v5, v60
	v_mov_b32_e32 v60, v15
	v_pk_mul_f32 v[14:15], v[18:19], v[48:49] op_sel_hi:[0,1]
	v_mov_b32_e32 v20, v16
	v_mov_b32_e32 v21, v62
	v_pk_mul_f32 v[14:15], v[14:15], v[20:21]
	v_pk_mul_f32 v[20:21], v[18:19], v[46:47] op_sel_hi:[0,1]
	v_mov_b32_e32 v62, v17
	v_pk_mul_f32 v[16:17], v[20:21], v[62:63]
	v_pk_mul_f32 v[20:21], v[18:19], v[42:43] op_sel_hi:[0,1]
	v_mov_b32_e32 v22, v6
	v_mov_b32_e32 v23, v24
	v_pk_mul_f32 v[2:3], v[18:19], v[52:53] op_sel_hi:[0,1]
	v_pk_mul_f32 v[20:21], v[20:21], v[22:23]
	v_pk_mul_f32 v[22:23], v[18:19], v[40:41] op_sel_hi:[0,1]
	v_mov_b32_e32 v24, v7
	v_pk_mul_f32 v[2:3], v[2:3], v[4:5]
	v_pk_mul_f32 v[4:5], v[18:19], v[50:51] op_sel_hi:[0,1]
	v_pk_mul_f32 v[6:7], v[22:23], v[24:25]
	v_pk_mul_f32 v[22:23], v[18:19], v[38:39] op_sel_hi:[0,1]
	v_mov_b32_e32 v25, v26
	v_pk_mul_f32 v[18:19], v[18:19], v[36:37] op_sel_hi:[0,1]
	v_mov_b32_e32 v26, v9
	v_mov_b32_e32 v24, v8
	v_pk_mul_f32 v[8:9], v[18:19], v[26:27]
	s_waitcnt vmcnt(1)
	v_mov_b32_e32 v18, v68
	v_mov_b32_e32 v19, v10
	v_pk_mul_f32 v[18:19], v[18:19], v[2:3]
	v_pk_mul_f32 v[4:5], v[4:5], v[60:61]
	v_pk_mul_f32 v[22:23], v[22:23], v[24:25]
	v_sub_f32_e32 v24, v18, v19
	v_mov_b32_e32 v18, v69
	v_mov_b32_e32 v19, v11
	v_pk_mul_f32 v[18:19], v[18:19], v[4:5]
	s_nop 0
	v_sub_f32_e32 v25, v18, v19
	v_mov_b32_e32 v18, v10
	v_mov_b32_e32 v19, v68
	v_pk_mul_f32 v[2:3], v[18:19], v[2:3]
	v_mov_b32_e32 v68, v11
	v_add_f32_e32 v10, v2, v3
	v_pk_mul_f32 v[2:3], v[68:69], v[4:5]
	v_cvt_pk_bf16_f32 v126, v24, v25
	s_nop 0
	v_add_f32_e32 v2, v2, v3
	v_cvt_pk_bf16_f32 v122, v10, v2
	v_mov_b32_e32 v2, v70
	v_mov_b32_e32 v3, v12
	v_pk_mul_f32 v[2:3], v[2:3], v[14:15]
	s_nop 0
	v_sub_f32_e32 v4, v2, v3
	v_mov_b32_e32 v2, v71
	v_mov_b32_e32 v3, v13
	v_pk_mul_f32 v[2:3], v[2:3], v[16:17]
	s_nop 0
	v_sub_f32_e32 v5, v2, v3
	v_mov_b32_e32 v2, v12
	v_mov_b32_e32 v3, v70
	v_pk_mul_f32 v[2:3], v[2:3], v[14:15]
	v_mov_b32_e32 v70, v13
	v_add_f32_e32 v10, v2, v3
	v_pk_mul_f32 v[2:3], v[70:71], v[16:17]
	v_cvt_pk_bf16_f32 v127, v4, v5
	s_nop 0
	v_add_f32_e32 v2, v2, v3
	v_cvt_pk_bf16_f32 v123, v10, v2
	v_mov_b32_e32 v2, v64
	s_waitcnt vmcnt(0)
	v_mov_b32_e32 v3, v54
	v_pk_mul_f32 v[2:3], v[2:3], v[20:21]
	s_nop 0
	v_sub_f32_e32 v4, v2, v3
	v_mov_b32_e32 v2, v65
	v_mov_b32_e32 v3, v55
	v_pk_mul_f32 v[2:3], v[2:3], v[6:7]
	s_nop 0
	v_sub_f32_e32 v5, v2, v3
	v_mov_b32_e32 v2, v54
	v_mov_b32_e32 v3, v64
	v_pk_mul_f32 v[2:3], v[2:3], v[20:21]
	v_mov_b32_e32 v64, v55
	v_add_f32_e32 v10, v2, v3
	v_pk_mul_f32 v[2:3], v[64:65], v[6:7]
	v_cvt_pk_bf16_f32 v128, v4, v5
	s_nop 0
	v_add_f32_e32 v2, v2, v3
	v_cvt_pk_bf16_f32 v124, v10, v2
	v_mov_b32_e32 v2, v66
	v_mov_b32_e32 v3, v56
	v_pk_mul_f32 v[2:3], v[2:3], v[22:23]
	s_nop 0
	v_sub_f32_e32 v4, v2, v3
	v_mov_b32_e32 v2, v67
	v_mov_b32_e32 v3, v57
	v_pk_mul_f32 v[2:3], v[2:3], v[8:9]
	s_nop 0
	v_sub_f32_e32 v5, v2, v3
	v_mov_b32_e32 v2, v56
	v_mov_b32_e32 v3, v66
	v_pk_mul_f32 v[2:3], v[2:3], v[22:23]
	v_mov_b32_e32 v66, v57
	v_add_f32_e32 v6, v2, v3
	v_pk_mul_f32 v[2:3], v[66:67], v[8:9]
	v_cvt_pk_bf16_f32 v129, v4, v5
	s_nop 0
	v_add_f32_e32 v2, v2, v3
	v_cvt_pk_bf16_f32 v125, v6, v2
.LBB0_408:
	v_and_b32_e32 v167, 63, v147
	v_and_b32_e32 v246, 15, v167
	v_lshrrev_b32_e32 v247, 4, v167
	v_lshlrev_b32_e32 v248, 13, v179
	v_add_u32_e32 v248, 0x10000, v248
	v_lshl_add_u32 v249, v177, 8, v248
	v_lshl_add_u32 v249, v178, 4, v249
	ds_write_b128 v249, v[102:105] offset:0
	ds_write_b128 v249, v[110:113] offset:32
	ds_write_b128 v249, v[98:101] offset:64
	ds_write_b128 v249, v[106:109] offset:96
	ds_write_b128 v249, v[118:121] offset:128
	ds_write_b128 v249, v[126:129] offset:160
	ds_write_b128 v249, v[114:117] offset:192
	ds_write_b128 v249, v[122:125] offset:224
	v_lshl_add_u32 v251, v246, 8, v248
	v_lshl_add_u32 v251, v247, 4, v251
	s_waitcnt lgkmcnt(0)
	ds_read_b128 v[98:101], v251 offset:0
	ds_read_b128 v[102:105], v251 offset:64
	ds_read_b128 v[106:109], v251 offset:128
	ds_read_b128 v[110:113], v251 offset:192
	ds_read_b128 v[114:117], v251 offset:4096
	ds_read_b128 v[118:121], v251 offset:4160
	ds_read_b128 v[122:125], v251 offset:4224
	ds_read_b128 v[126:129], v251 offset:4288
	v_lshlrev_b32_e32 v252, 4, v246
	v_lshlrev_b32_e32 v253, 4, v247
	v_lshlrev_b32_e32 v254, 8, v246
	v_or_b32_e32 v255, 0, v253
	v_xor_b32_e32 v255, v255, v252
	v_or_b32_e32 v183, v255, v254
	v_or_b32_e32 v255, 64, v253
	v_xor_b32_e32 v255, v255, v252
	v_or_b32_e32 v184, v255, v254
	v_or_b32_e32 v255, 128, v253
	v_xor_b32_e32 v255, v255, v252
	v_or_b32_e32 v185, v255, v254
	v_or_b32_e32 v255, 192, v253
	v_xor_b32_e32 v255, v255, v252
	v_or_b32_e32 v186, v255, v254
	v_lshrrev_b32_e32 v252, 1, v247
	v_lshlrev_b32_e32 v252, 11, v252
	v_and_b32_e32 v253, 1, v247
	v_lshl_add_u32 v252, v253, 8, v252
	v_lshrrev_b32_e32 v254, 2, v246
	v_lshl_add_u32 v252, v254, 6, v252
	v_and_b32_e32 v254, 3, v246
	v_lshl_add_u32 v252, v254, 3, v252
	v_lshl_add_u32 v191, v253, 5, v252
	v_xor_b32_e32 v253, 1, v253
	v_lshl_add_u32 v192, v253, 5, v252
	v_add_u32_e32 v191, 0x4000, v191
	v_add_u32_e32 v192, 0x4000, v192
	v_readfirstlane_b32 s42, v179
	v_mov_b32_e32 v170, v162
	v_mov_b32_e32 v172, v32
	v_mov_b32_e32 v171, v30
	v_mov_b32_e32 v173, v34
	v_mov_b32_e32 v2, 0
	v_mov_b32_e32 v3, 0
	v_mov_b32_e32 v4, 0
	v_mov_b32_e32 v5, 0
	v_mov_b32_e32 v6, 0
	v_mov_b32_e32 v7, 0
	v_mov_b32_e32 v8, 0
	v_mov_b32_e32 v9, 0
	v_mov_b32_e32 v10, 0
	v_mov_b32_e32 v11, 0
	v_mov_b32_e32 v12, 0
	v_mov_b32_e32 v13, 0
	v_mov_b32_e32 v14, 0
	v_mov_b32_e32 v15, 0
	v_mov_b32_e32 v16, 0
	v_mov_b32_e32 v17, 0
	v_mov_b32_e32 v18, 0
	v_mov_b32_e32 v19, 0
	v_mov_b32_e32 v20, 0
	v_mov_b32_e32 v21, 0
	v_mov_b32_e32 v22, 0
	v_mov_b32_e32 v23, 0
	v_mov_b32_e32 v24, 0
	v_mov_b32_e32 v25, 0
	v_mov_b32_e32 v26, 0
	v_mov_b32_e32 v27, 0
	v_mov_b32_e32 v28, 0
	v_mov_b32_e32 v29, 0
	v_mov_b32_e32 v30, 0
	v_mov_b32_e32 v31, 0
	v_mov_b32_e32 v32, 0
	v_mov_b32_e32 v33, 0
	v_mov_b32_e32 v34, 0
	v_mov_b32_e32 v35, 0
	v_mov_b32_e32 v36, 0
	v_mov_b32_e32 v37, 0
	v_mov_b32_e32 v38, 0
	v_mov_b32_e32 v39, 0
	v_mov_b32_e32 v40, 0
	v_mov_b32_e32 v41, 0
	v_mov_b32_e32 v42, 0
	v_mov_b32_e32 v43, 0
	v_mov_b32_e32 v44, 0
	v_mov_b32_e32 v45, 0
	v_mov_b32_e32 v46, 0
	v_mov_b32_e32 v47, 0
	v_mov_b32_e32 v48, 0
	v_mov_b32_e32 v49, 0
	v_mov_b32_e32 v50, 0
	v_mov_b32_e32 v51, 0
	v_mov_b32_e32 v52, 0
	v_mov_b32_e32 v53, 0
	v_mov_b32_e32 v54, 0
	v_mov_b32_e32 v55, 0
	v_mov_b32_e32 v56, 0
	v_mov_b32_e32 v57, 0
	v_mov_b32_e32 v58, 0
	v_mov_b32_e32 v59, 0
	v_mov_b32_e32 v60, 0
	v_mov_b32_e32 v61, 0
	v_mov_b32_e32 v62, 0
	v_mov_b32_e32 v63, 0
	v_mov_b32_e32 v64, 0
	v_mov_b32_e32 v65, 0
	v_mov_b32_e32 v182, 0
	v_mov_b32_e32 v195, 0
	s_cmp_lt_u32 s42, 4
	s_cbranch_scc1 .Lf16_noprio
	s_setprio 1
; __device__ __forceinline__ int v_rd_base(int lane) { return ((lane & 3) << 3) | (((lane >> 2) & 3) << 6) | (((lane >> 4) & 1) << 5) | (((lane >> 5) & 1) << 8); }
; #define ATT_WAIT_BAR() asm volatile("s_waitcnt vmcnt(0) lgkmcnt(0)\n\ts_barrier" ::: "memory")
; __device__ __forceinline__ void qkt(f32x16& p0, f32x16& p1, const bf16_t* Ks, const bf16x8* qr, int r32, int hi) {
;   p0 = f32x16{}; p1 = f32x16{};
;   for (int d0 = 0; d0 < 8; ++d0) { int cb = (d0 * 16 + hi * 8) * 2;
;     bf16x8 b0 = *reinterpret_cast<const bf16x8*>((const char*)Ks + KSWZ(r32, cb));
;     bf16x8 b1 = *reinterpret_cast<const bf16x8*>((const char*)Ks + KSWZ(32 + r32, cb));
;     p0 = __builtin_amdgcn_mfma_f32_32x32x16_bf16(b0, qr[d0], p0, 0, 0, 0);
;     p1 = __builtin_amdgcn_mfma_f32_32x32x16_bf16(b1, qr[d0], p1, 0, 0, 0); }
; __device__ __forceinline__ void attn_dma_body(const bf16_t* __restrict__ Qb, int ldq, int tpos0, const float* __restrict__ rope, const float* __restrict__ qgain, ...
;     ...
;   ATT_WAIT_BAR();
;   if (2 < NT) ATT_DMA(2, 2);
;   const int vb0 = (int)(uintptr_t)lds + 16384 + v_rd_base(lane);
;   f32x16 pA0, pA1, pB0, pB1; float mnA, mnB, alA, alB; bf16x8 pa0, pa1, pa2, pa3;
;   qkt(pA0, pA1, (const bf16_t*)lds, qr, r32, hi); partialSM(pA0, pA1, m_reg, mnA, alA);
;   const bool lead = __builtin_amdgcn_readfirstlane(wid) < 4;
.Lf16_noprio:
	s_waitcnt vmcnt(0) lgkmcnt(0)
	s_barrier
	s_add_u32 s2, s38, 0x8000
	s_addc_u32 s3, s39, 0
	s_add_u32 s4, s40, 0x8000
	s_addc_u32 s5, s41, 0
	s_add_i32 s6, s96, 0x10000
	s_mov_b32 m0, s6
	s_nop 0
	global_load_lds_dwordx4 v170, s[2:3]
	s_add_i32 m0, s6, 0x2000
	s_nop 0
	global_load_lds_dwordx4 v172, s[2:3]
	s_add_i32 m0, s6, 0x4000
	s_nop 0
	global_load_lds_dwordx4 v171, s[4:5]
	s_add_i32 m0, s6, 0x6000
	s_nop 0
	global_load_lds_dwordx4 v173, s[4:5]
	s_add_u32 s2, s2, 0x4000
	s_addc_u32 s3, s3, 0
	s_add_u32 s4, s4, 0x4000
	s_addc_u32 s5, s5, 0
	s_mov_b32 s36, 0
	v_add_u32_e32 v187, s36, v183
	v_add_u32_e32 v188, s36, v184
	v_add_u32_e32 v189, s36, v185
	v_add_u32_e32 v190, s36, v186
	ds_read_b128 v[146:149], v187 offset:0
	ds_read_b128 v[150:153], v187 offset:4096
	ds_read_b128 v[154:157], v187 offset:8192
	ds_read_b128 v[158:161], v187 offset:12288
	ds_read_b128 v[198:201], v188 offset:0
	ds_read_b128 v[202:205], v188 offset:4096
	ds_read_b128 v[206:209], v188 offset:8192
	ds_read_b128 v[210:213], v188 offset:12288
	s_waitcnt lgkmcnt(7)
	v_mfma_f32_16x16x32_bf16 v[66:69], v[146:149], v[98:101], 0
	v_mfma_f32_16x16x32_bf16 v[70:73], v[146:149], v[114:117], 0
	ds_read_b128 v[146:149], v189 offset:0
	s_waitcnt lgkmcnt(7)
	v_mfma_f32_16x16x32_bf16 v[74:77], v[150:153], v[98:101], 0
	v_mfma_f32_16x16x32_bf16 v[78:81], v[150:153], v[114:117], 0
	ds_read_b128 v[150:153], v189 offset:4096
	s_waitcnt lgkmcnt(7)
	v_mfma_f32_16x16x32_bf16 v[82:85], v[154:157], v[98:101], 0
	v_mfma_f32_16x16x32_bf16 v[86:89], v[154:157], v[114:117], 0
	ds_read_b128 v[154:157], v189 offset:8192
	s_waitcnt lgkmcnt(7)
	v_mfma_f32_16x16x32_bf16 v[90:93], v[158:161], v[98:101], 0
	v_mfma_f32_16x16x32_bf16 v[94:97], v[158:161], v[114:117], 0
	ds_read_b128 v[158:161], v189 offset:12288
	s_waitcnt lgkmcnt(7)
	v_mfma_f32_16x16x32_bf16 v[66:69], v[198:201], v[102:105], v[66:69]
	v_mfma_f32_16x16x32_bf16 v[70:73], v[198:201], v[118:121], v[70:73]
	ds_read_b128 v[198:201], v190 offset:0
	s_waitcnt lgkmcnt(7)
	v_mfma_f32_16x16x32_bf16 v[74:77], v[202:205], v[102:105], v[74:77]
	v_mfma_f32_16x16x32_bf16 v[78:81], v[202:205], v[118:121], v[78:81]
	ds_read_b128 v[202:205], v190 offset:4096
	s_waitcnt lgkmcnt(7)
	v_mfma_f32_16x16x32_bf16 v[82:85], v[206:209], v[102:105], v[82:85]
	v_mfma_f32_16x16x32_bf16 v[86:89], v[206:209], v[118:121], v[86:89]
	ds_read_b128 v[206:209], v190 offset:8192
	s_waitcnt lgkmcnt(7)
	v_mfma_f32_16x16x32_bf16 v[90:93], v[210:213], v[102:105], v[90:93]
	v_mfma_f32_16x16x32_bf16 v[94:97], v[210:213], v[118:121], v[94:97]
	ds_read_b128 v[210:213], v190 offset:12288
	s_waitcnt lgkmcnt(7)
	v_mfma_f32_16x16x32_bf16 v[66:69], v[146:149], v[106:109], v[66:69]
	v_mfma_f32_16x16x32_bf16 v[70:73], v[146:149], v[122:125], v[70:73]
	s_waitcnt lgkmcnt(6)
	v_mfma_f32_16x16x32_bf16 v[74:77], v[150:153], v[106:109], v[74:77]
	v_mfma_f32_16x16x32_bf16 v[78:81], v[150:153], v[122:125], v[78:81]
	s_waitcnt lgkmcnt(5)
	v_mfma_f32_16x16x32_bf16 v[82:85], v[154:157], v[106:109], v[82:85]
	v_mfma_f32_16x16x32_bf16 v[86:89], v[154:157], v[122:125], v[86:89]
	s_waitcnt lgkmcnt(4)
	v_mfma_f32_16x16x32_bf16 v[90:93], v[158:161], v[106:109], v[90:93]
	v_mfma_f32_16x16x32_bf16 v[94:97], v[158:161], v[122:125], v[94:97]
	s_waitcnt lgkmcnt(3)
	v_mfma_f32_16x16x32_bf16 v[66:69], v[198:201], v[110:113], v[66:69]
	v_mfma_f32_16x16x32_bf16 v[70:73], v[198:201], v[126:129], v[70:73]
	s_waitcnt lgkmcnt(2)
	v_mfma_f32_16x16x32_bf16 v[74:77], v[202:205], v[110:113], v[74:77]
	v_mfma_f32_16x16x32_bf16 v[78:81], v[202:205], v[126:129], v[78:81]
	s_waitcnt lgkmcnt(1)
	v_mfma_f32_16x16x32_bf16 v[82:85], v[206:209], v[110:113], v[82:85]
	v_mfma_f32_16x16x32_bf16 v[86:89], v[206:209], v[126:129], v[86:89]
	s_waitcnt lgkmcnt(0)
	v_mfma_f32_16x16x32_bf16 v[90:93], v[210:213], v[110:113], v[90:93]
	v_mfma_f32_16x16x32_bf16 v[94:97], v[210:213], v[126:129], v[94:97]
	s_nop 7
	v_exp_f32_e32 v66, v66
	v_exp_f32_e32 v67, v67
	v_exp_f32_e32 v68, v68
	v_exp_f32_e32 v69, v69
	v_exp_f32_e32 v70, v70
	v_exp_f32_e32 v71, v71
	v_exp_f32_e32 v72, v72
	v_exp_f32_e32 v73, v73
	v_exp_f32_e32 v74, v74
	v_exp_f32_e32 v75, v75
	v_exp_f32_e32 v76, v76
	v_exp_f32_e32 v77, v77
	v_exp_f32_e32 v78, v78
	v_exp_f32_e32 v79, v79
	v_exp_f32_e32 v80, v80
	v_exp_f32_e32 v81, v81
	v_exp_f32_e32 v82, v82
	v_exp_f32_e32 v83, v83
	v_exp_f32_e32 v84, v84
	v_exp_f32_e32 v85, v85
	v_exp_f32_e32 v86, v86
	v_exp_f32_e32 v87, v87
	v_exp_f32_e32 v88, v88
	v_exp_f32_e32 v89, v89
	v_exp_f32_e32 v90, v90
	v_exp_f32_e32 v91, v91
	v_exp_f32_e32 v92, v92
	v_exp_f32_e32 v93, v93
	v_exp_f32_e32 v94, v94
	v_exp_f32_e32 v95, v95
	v_exp_f32_e32 v96, v96
	v_exp_f32_e32 v97, v97
	v_add_f32_e32 v182, v182, v66
	v_add_f32_e32 v195, v195, v70
	v_add_f32_e32 v182, v182, v67
	v_add_f32_e32 v195, v195, v71
	v_add_f32_e32 v182, v182, v68
	v_add_f32_e32 v195, v195, v72
	v_add_f32_e32 v182, v182, v69
	v_add_f32_e32 v195, v195, v73
	v_add_f32_e32 v182, v182, v74
	v_add_f32_e32 v195, v195, v78
	v_add_f32_e32 v182, v182, v75
	v_add_f32_e32 v195, v195, v79
	v_add_f32_e32 v182, v182, v76
	v_add_f32_e32 v195, v195, v80
	v_add_f32_e32 v182, v182, v77
	v_add_f32_e32 v195, v195, v81
	v_add_f32_e32 v182, v182, v82
	v_add_f32_e32 v195, v195, v86
	v_add_f32_e32 v182, v182, v83
	v_add_f32_e32 v195, v195, v87
	v_add_f32_e32 v182, v182, v84
	v_add_f32_e32 v195, v195, v88
	v_add_f32_e32 v182, v182, v85
	v_add_f32_e32 v195, v195, v89
	v_add_f32_e32 v182, v182, v90
	v_add_f32_e32 v195, v195, v94
	v_add_f32_e32 v182, v182, v91
	v_add_f32_e32 v195, v195, v95
	v_add_f32_e32 v182, v182, v92
	v_add_f32_e32 v195, v195, v96
	v_add_f32_e32 v182, v182, v93
	v_add_f32_e32 v195, v195, v97
	v_cvt_pk_bf16_f32 v130, v66, v67
	v_cvt_pk_bf16_f32 v131, v68, v69
	v_cvt_pk_bf16_f32 v132, v74, v75
	v_cvt_pk_bf16_f32 v133, v76, v77
	v_cvt_pk_bf16_f32 v134, v82, v83
	v_cvt_pk_bf16_f32 v135, v84, v85
	v_cvt_pk_bf16_f32 v136, v90, v91
	v_cvt_pk_bf16_f32 v137, v92, v93
	v_cvt_pk_bf16_f32 v138, v70, v71
	v_cvt_pk_bf16_f32 v139, v72, v73
	v_cvt_pk_bf16_f32 v140, v78, v79
	v_cvt_pk_bf16_f32 v141, v80, v81
	v_cvt_pk_bf16_f32 v142, v86, v87
	v_cvt_pk_bf16_f32 v143, v88, v89
	v_cvt_pk_bf16_f32 v144, v94, v95
	v_cvt_pk_bf16_f32 v145, v96, v97
	s_mov_b32 s97, 1
; #define SBAR() __builtin_amdgcn_sched_barrier(0)
; #define RESC(a) do { if (__any((a) < 1.f)) { if (hi == 0) al_l[r32] = (a); asm volatile("s_waitcnt lgkmcnt(0)" ::: "memory"); \
;     for (int d = 0; d < 4; ++d) for (int r = 0; r < 16; ++r) o[d][r] *= al_l[crow(r, hi)]; } } while (0)
; #define RESC(a) do { if (__any((a) < 1.f)) { if (hi == 0) al_l[r32] = (a); asm volatile("s_waitcnt lgkmcnt(0)" ::: "memory"); \
;     for (int d = 0; d < 4; ++d) for (int r = 0; r < 16; ++r) o[d][r] *= al_l[crow(r, hi)]; } } while (0)
; #define ATT_SYNC(jn) do { ATT_WAIT_BAR(); if ((jn) < NT) ATT_DMA((jn), (jn) & 3); } while (0)
; __device__ __forceinline__ void attn_dma_body(const bf16_t* __restrict__ Qb, int ldq, int tpos0, const float* __restrict__ rope, const float* __restrict__ qgain, ...
;     ...
;   for (int j = 1; j + 1 < NT; j += 2) {
;     { SBAR(); qkt(pB0, pB1, (const bf16_t*)(lds + (j & 3) * SHM_SLOT), qr, r32, hi);
;       finishSM(pA0, pA1, alA, l_reg, pa0, pa1, pa2, pa3); s16x4 va[8]; pv_rd<0>(va, vb0 + ((j - 1) & 3) * (int)SHM_SLOT); SBAR();
;       if (!lead) ATT_SYNC(j + 2);
;       pv_d0_pre(o, vb0 + ((j - 1) & 3) * (int)SHM_SLOT, va, pa0, pa1, pa2, pa3); partialSM(pB0, pB1, m_reg, mnB, alB);
;       if (lead) ATT_SYNC(j + 2);
;       RESC(alB); }
;     { SBAR(); qkt(pA0, pA1, (const bf16_t*)(lds + ((j + 1) & 3) * SHM_SLOT), qr, r32, hi);
;       finishSM(pB0, pB1, alB, l_reg, pa0, pa1, pa2, pa3); s16x4 va[8]; pv_rd<0>(va, vb0 + (j & 3) * (int)SHM_SLOT); SBAR();
;       if (!lead) ATT_SYNC(j + 3);
;       pv_d0_pre(o, vb0 + (j & 3) * (int)SHM_SLOT, va, pa0, pa1, pa2, pa3); partialSM(pA0, pA1, m_reg, mnA, alA);
;       if (lead) ATT_SYNC(j + 3);
.Lf16_loop:
	s_lshl_b32 s36, s97, 15
	s_and_b32 s36, s36, 0x18000
	s_add_i32 s37, s36, 0x18000
	s_and_b32 s37, s37, 0x18000
	v_add_u32_e32 v187, s36, v183
	v_add_u32_e32 v188, s36, v184
	v_add_u32_e32 v189, s36, v185
	v_add_u32_e32 v190, s36, v186
	v_add_u32_e32 v193, s37, v191
	v_add_u32_e32 v194, s37, v192
	ds_read_b128 v[146:149], v187 offset:0
	ds_read_b128 v[150:153], v187 offset:4096
	ds_read_b128 v[154:157], v187 offset:8192
	ds_read_b128 v[158:161], v187 offset:12288
	ds_read_b128 v[198:201], v188 offset:0
	ds_read_b128 v[202:205], v188 offset:4096
	ds_read_b128 v[206:209], v188 offset:8192
	ds_read_b128 v[210:213], v188 offset:12288
	s_waitcnt lgkmcnt(7)
	v_mfma_f32_16x16x32_bf16 v[66:69], v[146:149], v[98:101], 0
	v_mfma_f32_16x16x32_bf16 v[70:73], v[146:149], v[114:117], 0
	ds_read_b128 v[146:149], v189 offset:0
	s_waitcnt lgkmcnt(7)
	v_mfma_f32_16x16x32_bf16 v[74:77], v[150:153], v[98:101], 0
	v_mfma_f32_16x16x32_bf16 v[78:81], v[150:153], v[114:117], 0
	ds_read_b128 v[150:153], v189 offset:4096
	s_waitcnt lgkmcnt(7)
	v_mfma_f32_16x16x32_bf16 v[82:85], v[154:157], v[98:101], 0
	v_mfma_f32_16x16x32_bf16 v[86:89], v[154:157], v[114:117], 0
	ds_read_b128 v[154:157], v189 offset:8192
	s_waitcnt lgkmcnt(7)
	v_mfma_f32_16x16x32_bf16 v[90:93], v[158:161], v[98:101], 0
	v_mfma_f32_16x16x32_bf16 v[94:97], v[158:161], v[114:117], 0
	ds_read_b128 v[158:161], v189 offset:12288
	s_waitcnt lgkmcnt(7)
	v_mfma_f32_16x16x32_bf16 v[66:69], v[198:201], v[102:105], v[66:69]
	v_mfma_f32_16x16x32_bf16 v[70:73], v[198:201], v[118:121], v[70:73]
	ds_read_b128 v[198:201], v190 offset:0
	s_waitcnt lgkmcnt(7)
	v_mfma_f32_16x16x32_bf16 v[74:77], v[202:205], v[102:105], v[74:77]
	v_mfma_f32_16x16x32_bf16 v[78:81], v[202:205], v[118:121], v[78:81]
	ds_read_b128 v[202:205], v190 offset:4096
	s_waitcnt lgkmcnt(7)
	v_mfma_f32_16x16x32_bf16 v[82:85], v[206:209], v[102:105], v[82:85]
	v_mfma_f32_16x16x32_bf16 v[86:89], v[206:209], v[118:121], v[86:89]
	ds_read_b128 v[206:209], v190 offset:8192
	s_waitcnt lgkmcnt(7)
	v_mfma_f32_16x16x32_bf16 v[90:93], v[210:213], v[102:105], v[90:93]
	v_mfma_f32_16x16x32_bf16 v[94:97], v[210:213], v[118:121], v[94:97]
	ds_read_b128 v[210:213], v190 offset:12288
	s_waitcnt lgkmcnt(7)
	v_mfma_f32_16x16x32_bf16 v[66:69], v[146:149], v[106:109], v[66:69]
	v_mfma_f32_16x16x32_bf16 v[70:73], v[146:149], v[122:125], v[70:73]
	s_waitcnt lgkmcnt(6)
	v_mfma_f32_16x16x32_bf16 v[74:77], v[150:153], v[106:109], v[74:77]
	v_mfma_f32_16x16x32_bf16 v[78:81], v[150:153], v[122:125], v[78:81]
	s_waitcnt lgkmcnt(5)
	v_mfma_f32_16x16x32_bf16 v[82:85], v[154:157], v[106:109], v[82:85]
	v_mfma_f32_16x16x32_bf16 v[86:89], v[154:157], v[122:125], v[86:89]
	s_waitcnt lgkmcnt(4)
	v_mfma_f32_16x16x32_bf16 v[90:93], v[158:161], v[106:109], v[90:93]
	v_mfma_f32_16x16x32_bf16 v[94:97], v[158:161], v[122:125], v[94:97]
	s_waitcnt lgkmcnt(3)
	v_mfma_f32_16x16x32_bf16 v[66:69], v[198:201], v[110:113], v[66:69]
	v_mfma_f32_16x16x32_bf16 v[70:73], v[198:201], v[126:129], v[70:73]
	ds_read_b64_tr_b16 v[214:215], v193 offset:0
	ds_read_b64_tr_b16 v[216:217], v193 offset:4096
	ds_read_b64_tr_b16 v[218:219], v194 offset:0
	ds_read_b64_tr_b16 v[220:221], v194 offset:4096
	ds_read_b64_tr_b16 v[222:223], v193 offset:512
	ds_read_b64_tr_b16 v[224:225], v193 offset:4608
	ds_read_b64_tr_b16 v[226:227], v194 offset:512
	ds_read_b64_tr_b16 v[228:229], v194 offset:4608
	s_waitcnt lgkmcnt(10)
	v_mfma_f32_16x16x32_bf16 v[74:77], v[202:205], v[110:113], v[74:77]
	v_mfma_f32_16x16x32_bf16 v[78:81], v[202:205], v[126:129], v[78:81]
	s_waitcnt lgkmcnt(9)
	v_mfma_f32_16x16x32_bf16 v[82:85], v[206:209], v[110:113], v[82:85]
	v_mfma_f32_16x16x32_bf16 v[86:89], v[206:209], v[126:129], v[86:89]
	s_waitcnt lgkmcnt(8)
	v_mfma_f32_16x16x32_bf16 v[90:93], v[210:213], v[110:113], v[90:93]
	v_mfma_f32_16x16x32_bf16 v[94:97], v[210:213], v[126:129], v[94:97]
	s_cmp_lt_u32 s42, 4
	s_cbranch_scc1 .Lf16_a
	s_cmp_ge_u32 s97, 131
	s_cbranch_scc1 .Lf16_se_nl
	s_waitcnt vmcnt(0) lgkmcnt(0)
	s_barrier
	s_cmp_ge_u32 s97, 130
	s_cbranch_scc1 .Lf16_se_nl
	s_add_i32 s6, s36, 0x10000
	s_and_b32 s6, s6, 0x18000
	s_add_i32 s6, s6, s96
	s_mov_b32 m0, s6
	s_nop 0
	global_load_lds_dwordx4 v170, s[2:3]
	s_add_i32 m0, s6, 0x2000
	s_nop 0
	global_load_lds_dwordx4 v172, s[2:3]
	s_add_i32 m0, s6, 0x4000
	s_nop 0
	global_load_lds_dwordx4 v171, s[4:5]
	s_add_i32 m0, s6, 0x6000
	s_nop 0
	global_load_lds_dwordx4 v173, s[4:5]
	s_add_u32 s2, s2, 0x4000
	s_addc_u32 s3, s3, 0
	s_add_u32 s4, s4, 0x4000
	s_addc_u32 s5, s5, 0
; #define SBAR() __builtin_amdgcn_sched_barrier(0)
; #define RESC(a) do { if (__any((a) < 1.f)) { if (hi == 0) al_l[r32] = (a); asm volatile("s_waitcnt lgkmcnt(0)" ::: "memory"); \
;     for (int d = 0; d < 4; ++d) for (int r = 0; r < 16; ++r) o[d][r] *= al_l[crow(r, hi)]; } } while (0)
; #define RESC(a) do { if (__any((a) < 1.f)) { if (hi == 0) al_l[r32] = (a); asm volatile("s_waitcnt lgkmcnt(0)" ::: "memory"); \
;     for (int d = 0; d < 4; ++d) for (int r = 0; r < 16; ++r) o[d][r] *= al_l[crow(r, hi)]; } } while (0)
; #define ATT_SYNC(jn) do { ATT_WAIT_BAR(); if ((jn) < NT) ATT_DMA((jn), (jn) & 3); } while (0)
; __device__ __forceinline__ void attn_dma_body(const bf16_t* __restrict__ Qb, int ldq, int tpos0, const float* __restrict__ rope, const float* __restrict__ qgain, ...
;     ...
;   for (int j = 1; j + 1 < NT; j += 2) {
;     { SBAR(); qkt(pB0, pB1, (const bf16_t*)(lds + (j & 3) * SHM_SLOT), qr, r32, hi);
;       finishSM(pA0, pA1, alA, l_reg, pa0, pa1, pa2, pa3); s16x4 va[8]; pv_rd<0>(va, vb0 + ((j - 1) & 3) * (int)SHM_SLOT); SBAR();
;       if (!lead) ATT_SYNC(j + 2);
;       pv_d0_pre(o, vb0 + ((j - 1) & 3) * (int)SHM_SLOT, va, pa0, pa1, pa2, pa3); partialSM(pB0, pB1, m_reg, mnB, alB);
;       if (lead) ATT_SYNC(j + 2);
;       RESC(alB); }
;     { SBAR(); qkt(pA0, pA1, (const bf16_t*)(lds + ((j + 1) & 3) * SHM_SLOT), qr, r32, hi);
;       finishSM(pB0, pB1, alB, l_reg, pa0, pa1, pa2, pa3); s16x4 va[8]; pv_rd<0>(va, vb0 + (j & 3) * (int)SHM_SLOT); SBAR();
;       if (!lead) ATT_SYNC(j + 3);
;       pv_d0_pre(o, vb0 + (j & 3) * (int)SHM_SLOT, va, pa0, pa1, pa2, pa3); partialSM(pA0, pA1, m_reg, mnA, alA);
;       if (lead) ATT_SYNC(j + 3);
;       RESC(alA); }
.Lf16_se_nl:
.Lf16_a:
	s_waitcnt lgkmcnt(6)
	v_mfma_f32_16x16x32_bf16 v[2:5], v[214:217], v[130:133], v[2:5]
	v_mfma_f32_16x16x32_bf16 v[6:9], v[214:217], v[138:141], v[6:9]
	ds_read_b64_tr_b16 v[230:231], v193 offset:1024
	ds_read_b64_tr_b16 v[232:233], v193 offset:5120
	s_waitcnt lgkmcnt(6)
	v_mfma_f32_16x16x32_bf16 v[10:13], v[218:221], v[130:133], v[10:13]
	v_mfma_f32_16x16x32_bf16 v[14:17], v[218:221], v[138:141], v[14:17]
	ds_read_b64_tr_b16 v[234:235], v194 offset:1024
	ds_read_b64_tr_b16 v[236:237], v194 offset:5120
	s_waitcnt lgkmcnt(6)
	v_mfma_f32_16x16x32_bf16 v[18:21], v[222:225], v[130:133], v[18:21]
	v_mfma_f32_16x16x32_bf16 v[22:25], v[222:225], v[138:141], v[22:25]
	ds_read_b64_tr_b16 v[238:239], v193 offset:1536
	ds_read_b64_tr_b16 v[240:241], v193 offset:5632
	s_waitcnt lgkmcnt(6)
	v_mfma_f32_16x16x32_bf16 v[26:29], v[226:229], v[130:133], v[26:29]
	v_mfma_f32_16x16x32_bf16 v[30:33], v[226:229], v[138:141], v[30:33]
	ds_read_b64_tr_b16 v[242:243], v194 offset:1536
	ds_read_b64_tr_b16 v[244:245], v194 offset:5632
	s_waitcnt lgkmcnt(6)
	v_mfma_f32_16x16x32_bf16 v[34:37], v[230:233], v[130:133], v[34:37]
	v_mfma_f32_16x16x32_bf16 v[38:41], v[230:233], v[138:141], v[38:41]
	ds_read_b64_tr_b16 v[214:215], v193 offset:8192
	ds_read_b64_tr_b16 v[216:217], v193 offset:12288
	s_waitcnt lgkmcnt(6)
	v_mfma_f32_16x16x32_bf16 v[42:45], v[234:237], v[130:133], v[42:45]
	v_mfma_f32_16x16x32_bf16 v[46:49], v[234:237], v[138:141], v[46:49]
	ds_read_b64_tr_b16 v[218:219], v194 offset:8192
	ds_read_b64_tr_b16 v[220:221], v194 offset:12288
	s_waitcnt lgkmcnt(6)
	v_mfma_f32_16x16x32_bf16 v[50:53], v[238:241], v[130:133], v[50:53]
	v_mfma_f32_16x16x32_bf16 v[54:57], v[238:241], v[138:141], v[54:57]
	ds_read_b64_tr_b16 v[222:223], v193 offset:8704
	ds_read_b64_tr_b16 v[224:225], v193 offset:12800
	s_waitcnt lgkmcnt(6)
	v_mfma_f32_16x16x32_bf16 v[58:61], v[242:245], v[130:133], v[58:61]
	v_mfma_f32_16x16x32_bf16 v[62:65], v[242:245], v[138:141], v[62:65]
	ds_read_b64_tr_b16 v[226:227], v194 offset:8704
	ds_read_b64_tr_b16 v[228:229], v194 offset:12800
	s_waitcnt lgkmcnt(6)
	v_mfma_f32_16x16x32_bf16 v[2:5], v[214:217], v[134:137], v[2:5]
	v_mfma_f32_16x16x32_bf16 v[6:9], v[214:217], v[142:145], v[6:9]
	ds_read_b64_tr_b16 v[230:231], v193 offset:9216
	ds_read_b64_tr_b16 v[232:233], v193 offset:13312
	s_waitcnt lgkmcnt(6)
	v_mfma_f32_16x16x32_bf16 v[10:13], v[218:221], v[134:137], v[10:13]
	v_mfma_f32_16x16x32_bf16 v[14:17], v[218:221], v[142:145], v[14:17]
	ds_read_b64_tr_b16 v[234:235], v194 offset:9216
	ds_read_b64_tr_b16 v[236:237], v194 offset:13312
	s_waitcnt lgkmcnt(6)
	v_mfma_f32_16x16x32_bf16 v[18:21], v[222:225], v[134:137], v[18:21]
	v_mfma_f32_16x16x32_bf16 v[22:25], v[222:225], v[142:145], v[22:25]
	ds_read_b64_tr_b16 v[238:239], v193 offset:9728
	ds_read_b64_tr_b16 v[240:241], v193 offset:13824
	s_waitcnt lgkmcnt(6)
	v_mfma_f32_16x16x32_bf16 v[26:29], v[226:229], v[134:137], v[26:29]
	v_mfma_f32_16x16x32_bf16 v[30:33], v[226:229], v[142:145], v[30:33]
	ds_read_b64_tr_b16 v[242:243], v194 offset:9728
	ds_read_b64_tr_b16 v[244:245], v194 offset:13824
	s_waitcnt lgkmcnt(6)
	v_mfma_f32_16x16x32_bf16 v[34:37], v[230:233], v[134:137], v[34:37]
	v_mfma_f32_16x16x32_bf16 v[38:41], v[230:233], v[142:145], v[38:41]
	s_waitcnt lgkmcnt(4)
	v_mfma_f32_16x16x32_bf16 v[42:45], v[234:237], v[134:137], v[42:45]
	v_mfma_f32_16x16x32_bf16 v[46:49], v[234:237], v[142:145], v[46:49]
	s_waitcnt lgkmcnt(2)
	v_mfma_f32_16x16x32_bf16 v[50:53], v[238:241], v[134:137], v[50:53]
	v_mfma_f32_16x16x32_bf16 v[54:57], v[238:241], v[142:145], v[54:57]
	s_waitcnt lgkmcnt(0)
	v_mfma_f32_16x16x32_bf16 v[58:61], v[242:245], v[134:137], v[58:61]
	v_mfma_f32_16x16x32_bf16 v[62:65], v[242:245], v[142:145], v[62:65]
	s_cmp_lt_u32 s42, 4
	s_cbranch_scc0 .Lf16_b
	s_cmp_ge_u32 s97, 131
	s_cbranch_scc1 .Lf16_se_l
	s_waitcnt vmcnt(0) lgkmcnt(0)
	s_barrier
	s_cmp_ge_u32 s97, 130
	s_cbranch_scc1 .Lf16_se_l
	s_add_i32 s6, s36, 0x10000
	s_and_b32 s6, s6, 0x18000
	s_add_i32 s6, s6, s96
	s_mov_b32 m0, s6
	s_nop 0
	global_load_lds_dwordx4 v170, s[2:3]
	s_add_i32 m0, s6, 0x2000
	s_nop 0
	global_load_lds_dwordx4 v172, s[2:3]
	s_add_i32 m0, s6, 0x4000
	s_nop 0
	global_load_lds_dwordx4 v171, s[4:5]
	s_add_i32 m0, s6, 0x6000
	s_nop 0
	global_load_lds_dwordx4 v173, s[4:5]
	s_add_u32 s2, s2, 0x4000
	s_addc_u32 s3, s3, 0
	s_add_u32 s4, s4, 0x4000
	s_addc_u32 s5, s5, 0
; #define SBAR() __builtin_amdgcn_sched_barrier(0)
; #define RESC(a) do { if (__any((a) < 1.f)) { if (hi == 0) al_l[r32] = (a); asm volatile("s_waitcnt lgkmcnt(0)" ::: "memory"); \
;     for (int d = 0; d < 4; ++d) for (int r = 0; r < 16; ++r) o[d][r] *= al_l[crow(r, hi)]; } } while (0)
; #define RESC(a) do { if (__any((a) < 1.f)) { if (hi == 0) al_l[r32] = (a); asm volatile("s_waitcnt lgkmcnt(0)" ::: "memory"); \
;     for (int d = 0; d < 4; ++d) for (int r = 0; r < 16; ++r) o[d][r] *= al_l[crow(r, hi)]; } } while (0)
; #define ATT_SYNC(jn) do { ATT_WAIT_BAR(); if ((jn) < NT) ATT_DMA((jn), (jn) & 3); } while (0)
; __device__ __forceinline__ void attn_dma_body(const bf16_t* __restrict__ Qb, int ldq, int tpos0, const float* __restrict__ rope, const float* __restrict__ qgain, ...
;     ...
;   for (int j = 1; j + 1 < NT; j += 2) {
;     { SBAR(); qkt(pB0, pB1, (const bf16_t*)(lds + (j & 3) * SHM_SLOT), qr, r32, hi);
;       finishSM(pA0, pA1, alA, l_reg, pa0, pa1, pa2, pa3); s16x4 va[8]; pv_rd<0>(va, vb0 + ((j - 1) & 3) * (int)SHM_SLOT); SBAR();
;       if (!lead) ATT_SYNC(j + 2);
;       pv_d0_pre(o, vb0 + ((j - 1) & 3) * (int)SHM_SLOT, va, pa0, pa1, pa2, pa3); partialSM(pB0, pB1, m_reg, mnB, alB);
;       if (lead) ATT_SYNC(j + 2);
;       RESC(alB); }
;     { SBAR(); qkt(pA0, pA1, (const bf16_t*)(lds + ((j + 1) & 3) * SHM_SLOT), qr, r32, hi);
;       finishSM(pB0, pB1, alB, l_reg, pa0, pa1, pa2, pa3); s16x4 va[8]; pv_rd<0>(va, vb0 + (j & 3) * (int)SHM_SLOT); SBAR();
;       if (!lead) ATT_SYNC(j + 3);
;       pv_d0_pre(o, vb0 + (j & 3) * (int)SHM_SLOT, va, pa0, pa1, pa2, pa3); partialSM(pA0, pA1, m_reg, mnA, alA);
;       if (lead) ATT_SYNC(j + 3);
;       RESC(alA); }
;   }
;     ...
;   { SBAR(); qkt(pB0, pB1, (const bf16_t*)(lds + ((NT - 1) & 3) * SHM_SLOT), qr, r32, hi);
;     finishSM(pA0, pA1, alA, l_reg, pa0, pa1, pa2, pa3); SBAR();
;     pv_d0(o, vb0 + ((NT - 2) & 3) * (int)SHM_SLOT, pa0, pa1, pa2, pa3); partialSM(pB0, pB1, m_reg, mnB, alB);
;     RESC(alB);
;     finishSM(pB0, pB1, alB, l_reg, pa0, pa1, pa2, pa3); SBAR();
;     pv_d0(o, vb0 + ((NT - 1) & 3) * (int)SHM_SLOT, pa0, pa1, pa2, pa3); }
.Lf16_se_l:
.Lf16_b:
	v_exp_f32_e32 v66, v66
	v_exp_f32_e32 v67, v67
	v_exp_f32_e32 v68, v68
	v_exp_f32_e32 v69, v69
	v_exp_f32_e32 v70, v70
	v_exp_f32_e32 v71, v71
	v_exp_f32_e32 v72, v72
	v_exp_f32_e32 v73, v73
	v_exp_f32_e32 v74, v74
	v_exp_f32_e32 v75, v75
	v_exp_f32_e32 v76, v76
	v_exp_f32_e32 v77, v77
	v_exp_f32_e32 v78, v78
	v_exp_f32_e32 v79, v79
	v_exp_f32_e32 v80, v80
	v_exp_f32_e32 v81, v81
	v_exp_f32_e32 v82, v82
	v_exp_f32_e32 v83, v83
	v_exp_f32_e32 v84, v84
	v_exp_f32_e32 v85, v85
	v_exp_f32_e32 v86, v86
	v_exp_f32_e32 v87, v87
	v_exp_f32_e32 v88, v88
	v_exp_f32_e32 v89, v89
	v_exp_f32_e32 v90, v90
	v_exp_f32_e32 v91, v91
	v_exp_f32_e32 v92, v92
	v_exp_f32_e32 v93, v93
	v_exp_f32_e32 v94, v94
	v_exp_f32_e32 v95, v95
	v_exp_f32_e32 v96, v96
	v_exp_f32_e32 v97, v97
	v_add_f32_e32 v182, v182, v66
	v_add_f32_e32 v195, v195, v70
	v_add_f32_e32 v182, v182, v67
	v_add_f32_e32 v195, v195, v71
	v_add_f32_e32 v182, v182, v68
	v_add_f32_e32 v195, v195, v72
	v_add_f32_e32 v182, v182, v69
	v_add_f32_e32 v195, v195, v73
	v_add_f32_e32 v182, v182, v74
	v_add_f32_e32 v195, v195, v78
	v_add_f32_e32 v182, v182, v75
	v_add_f32_e32 v195, v195, v79
	v_add_f32_e32 v182, v182, v76
	v_add_f32_e32 v195, v195, v80
	v_add_f32_e32 v182, v182, v77
	v_add_f32_e32 v195, v195, v81
	v_add_f32_e32 v182, v182, v82
	v_add_f32_e32 v195, v195, v86
	v_add_f32_e32 v182, v182, v83
	v_add_f32_e32 v195, v195, v87
	v_add_f32_e32 v182, v182, v84
	v_add_f32_e32 v195, v195, v88
	v_add_f32_e32 v182, v182, v85
	v_add_f32_e32 v195, v195, v89
	v_add_f32_e32 v182, v182, v90
	v_add_f32_e32 v195, v195, v94
	v_add_f32_e32 v182, v182, v91
	v_add_f32_e32 v195, v195, v95
	v_add_f32_e32 v182, v182, v92
	v_add_f32_e32 v195, v195, v96
	v_add_f32_e32 v182, v182, v93
	v_add_f32_e32 v195, v195, v97
	v_cvt_pk_bf16_f32 v130, v66, v67
	v_cvt_pk_bf16_f32 v131, v68, v69
	v_cvt_pk_bf16_f32 v132, v74, v75
	v_cvt_pk_bf16_f32 v133, v76, v77
	v_cvt_pk_bf16_f32 v134, v82, v83
	v_cvt_pk_bf16_f32 v135, v84, v85
	v_cvt_pk_bf16_f32 v136, v90, v91
	v_cvt_pk_bf16_f32 v137, v92, v93
	v_cvt_pk_bf16_f32 v138, v70, v71
	v_cvt_pk_bf16_f32 v139, v72, v73
	v_cvt_pk_bf16_f32 v140, v78, v79
	v_cvt_pk_bf16_f32 v141, v80, v81
	v_cvt_pk_bf16_f32 v142, v86, v87
	v_cvt_pk_bf16_f32 v143, v88, v89
	v_cvt_pk_bf16_f32 v144, v94, v95
	v_cvt_pk_bf16_f32 v145, v96, v97
	s_add_i32 s97, s97, 1
	s_cmp_lt_u32 s97, 132
	s_cbranch_scc1 .Lf16_loop
	s_mov_b32 s37, 0x18000
	v_add_u32_e32 v193, s37, v191
	v_add_u32_e32 v194, s37, v192
	ds_read_b64_tr_b16 v[214:215], v193 offset:0
	ds_read_b64_tr_b16 v[216:217], v193 offset:4096
	ds_read_b64_tr_b16 v[218:219], v194 offset:0
	ds_read_b64_tr_b16 v[220:221], v194 offset:4096
	ds_read_b64_tr_b16 v[222:223], v193 offset:512
	ds_read_b64_tr_b16 v[224:225], v193 offset:4608
	ds_read_b64_tr_b16 v[226:227], v194 offset:512
	ds_read_b64_tr_b16 v[228:229], v194 offset:4608
	s_waitcnt lgkmcnt(6)
	v_mfma_f32_16x16x32_bf16 v[2:5], v[214:217], v[130:133], v[2:5]
	v_mfma_f32_16x16x32_bf16 v[6:9], v[214:217], v[138:141], v[6:9]
	ds_read_b64_tr_b16 v[230:231], v193 offset:1024
	ds_read_b64_tr_b16 v[232:233], v193 offset:5120
	s_waitcnt lgkmcnt(6)
	v_mfma_f32_16x16x32_bf16 v[10:13], v[218:221], v[130:133], v[10:13]
	v_mfma_f32_16x16x32_bf16 v[14:17], v[218:221], v[138:141], v[14:17]
	ds_read_b64_tr_b16 v[234:235], v194 offset:1024
	ds_read_b64_tr_b16 v[236:237], v194 offset:5120
	s_waitcnt lgkmcnt(6)
	v_mfma_f32_16x16x32_bf16 v[18:21], v[222:225], v[130:133], v[18:21]
	v_mfma_f32_16x16x32_bf16 v[22:25], v[222:225], v[138:141], v[22:25]
	ds_read_b64_tr_b16 v[238:239], v193 offset:1536
	ds_read_b64_tr_b16 v[240:241], v193 offset:5632
	s_waitcnt lgkmcnt(6)
	v_mfma_f32_16x16x32_bf16 v[26:29], v[226:229], v[130:133], v[26:29]
	v_mfma_f32_16x16x32_bf16 v[30:33], v[226:229], v[138:141], v[30:33]
	ds_read_b64_tr_b16 v[242:243], v194 offset:1536
	ds_read_b64_tr_b16 v[244:245], v194 offset:5632
	s_waitcnt lgkmcnt(6)
	v_mfma_f32_16x16x32_bf16 v[34:37], v[230:233], v[130:133], v[34:37]
	v_mfma_f32_16x16x32_bf16 v[38:41], v[230:233], v[138:141], v[38:41]
	ds_read_b64_tr_b16 v[214:215], v193 offset:8192
	ds_read_b64_tr_b16 v[216:217], v193 offset:12288
	s_waitcnt lgkmcnt(6)
	v_mfma_f32_16x16x32_bf16 v[42:45], v[234:237], v[130:133], v[42:45]
	v_mfma_f32_16x16x32_bf16 v[46:49], v[234:237], v[138:141], v[46:49]
	ds_read_b64_tr_b16 v[218:219], v194 offset:8192
	ds_read_b64_tr_b16 v[220:221], v194 offset:12288
	s_waitcnt lgkmcnt(6)
	v_mfma_f32_16x16x32_bf16 v[50:53], v[238:241], v[130:133], v[50:53]
	v_mfma_f32_16x16x32_bf16 v[54:57], v[238:241], v[138:141], v[54:57]
	ds_read_b64_tr_b16 v[222:223], v193 offset:8704
	ds_read_b64_tr_b16 v[224:225], v193 offset:12800
	s_waitcnt lgkmcnt(6)
	v_mfma_f32_16x16x32_bf16 v[58:61], v[242:245], v[130:133], v[58:61]
	v_mfma_f32_16x16x32_bf16 v[62:65], v[242:245], v[138:141], v[62:65]
	ds_read_b64_tr_b16 v[226:227], v194 offset:8704
	ds_read_b64_tr_b16 v[228:229], v194 offset:12800
	s_waitcnt lgkmcnt(6)
	v_mfma_f32_16x16x32_bf16 v[2:5], v[214:217], v[134:137], v[2:5]
	v_mfma_f32_16x16x32_bf16 v[6:9], v[214:217], v[142:145], v[6:9]
	ds_read_b64_tr_b16 v[230:231], v193 offset:9216
	ds_read_b64_tr_b16 v[232:233], v193 offset:13312
	s_waitcnt lgkmcnt(6)
	v_mfma_f32_16x16x32_bf16 v[10:13], v[218:221], v[134:137], v[10:13]
	v_mfma_f32_16x16x32_bf16 v[14:17], v[218:221], v[142:145], v[14:17]
	ds_read_b64_tr_b16 v[234:235], v194 offset:9216
	ds_read_b64_tr_b16 v[236:237], v194 offset:13312
	s_waitcnt lgkmcnt(6)
	v_mfma_f32_16x16x32_bf16 v[18:21], v[222:225], v[134:137], v[18:21]
	v_mfma_f32_16x16x32_bf16 v[22:25], v[222:225], v[142:145], v[22:25]
	ds_read_b64_tr_b16 v[238:239], v193 offset:9728
	ds_read_b64_tr_b16 v[240:241], v193 offset:13824
	s_waitcnt lgkmcnt(6)
; #define SBAR() __builtin_amdgcn_sched_barrier(0)
; __device__ __forceinline__ int crow(int r, int hi) { return (r & 3) + 8 * (r >> 2) + 4 * hi; }
; #define RESC(a) do { if (__any((a) < 1.f)) { if (hi == 0) al_l[r32] = (a); asm volatile("s_waitcnt lgkmcnt(0)" ::: "memory"); \
;     for (int d = 0; d < 4; ++d) for (int r = 0; r < 16; ++r) o[d][r] *= al_l[crow(r, hi)]; } } while (0)
; #define RESC(a) do { if (__any((a) < 1.f)) { if (hi == 0) al_l[r32] = (a); asm volatile("s_waitcnt lgkmcnt(0)" ::: "memory"); \
;     for (int d = 0; d < 4; ++d) for (int r = 0; r < 16; ++r) o[d][r] *= al_l[crow(r, hi)]; } } while (0)
; __device__ __forceinline__ void attn_dma_body(const bf16_t* __restrict__ Qb, int ldq, int tpos0, const float* __restrict__ rope, const float* __restrict__ qgain, ...
;     ...
;   { SBAR(); qkt(pB0, pB1, (const bf16_t*)(lds + ((NT - 1) & 3) * SHM_SLOT), qr, r32, hi);
;     finishSM(pA0, pA1, alA, l_reg, pa0, pa1, pa2, pa3); SBAR();
;     pv_d0(o, vb0 + ((NT - 2) & 3) * (int)SHM_SLOT, pa0, pa1, pa2, pa3); partialSM(pB0, pB1, m_reg, mnB, alB);
;     RESC(alB);
;     finishSM(pB0, pB1, alB, l_reg, pa0, pa1, pa2, pa3); SBAR();
;     pv_d0(o, vb0 + ((NT - 1) & 3) * (int)SHM_SLOT, pa0, pa1, pa2, pa3); }
;   if (hi == 0) li_l[r32] = l_reg; asm volatile("s_waitcnt lgkmcnt(0)" ::: "memory");
;   float rli[16];
; #pragma unroll
;   for (int r = 0; r < 16; ++r) rli[r] = __builtin_amdgcn_rcpf(li_l[crow(r, hi)]);
	v_mfma_f32_16x16x32_bf16 v[26:29], v[226:229], v[134:137], v[26:29]
	v_mfma_f32_16x16x32_bf16 v[30:33], v[226:229], v[142:145], v[30:33]
	ds_read_b64_tr_b16 v[242:243], v194 offset:9728
	ds_read_b64_tr_b16 v[244:245], v194 offset:13824
	s_waitcnt lgkmcnt(6)
	v_mfma_f32_16x16x32_bf16 v[34:37], v[230:233], v[134:137], v[34:37]
	v_mfma_f32_16x16x32_bf16 v[38:41], v[230:233], v[142:145], v[38:41]
	s_waitcnt lgkmcnt(4)
	v_mfma_f32_16x16x32_bf16 v[42:45], v[234:237], v[134:137], v[42:45]
	v_mfma_f32_16x16x32_bf16 v[46:49], v[234:237], v[142:145], v[46:49]
	s_waitcnt lgkmcnt(2)
	v_mfma_f32_16x16x32_bf16 v[50:53], v[238:241], v[134:137], v[50:53]
	v_mfma_f32_16x16x32_bf16 v[54:57], v[238:241], v[142:145], v[54:57]
	s_waitcnt lgkmcnt(0)
	v_mfma_f32_16x16x32_bf16 v[58:61], v[242:245], v[134:137], v[58:61]
	v_mfma_f32_16x16x32_bf16 v[62:65], v[242:245], v[142:145], v[62:65]
	v_mov_b32_e32 v246, v182
	s_nop 1
	v_permlane32_swap_b32_e32 v182, v246
	v_add_f32_e32 v182, v182, v246
	v_mov_b32_e32 v246, v182
	s_nop 1
	v_permlane16_swap_b32_e32 v182, v246
	v_add_f32_e32 v182, v182, v246
	v_mov_b32_e32 v246, v195
	s_nop 1
	v_permlane32_swap_b32_e32 v195, v246
	v_add_f32_e32 v195, v195, v246
	v_mov_b32_e32 v246, v195
	s_nop 1
	v_permlane16_swap_b32_e32 v195, v246
	v_add_f32_e32 v195, v195, v246
	v_rcp_f32_e32 v182, v182
	v_rcp_f32_e32 v195, v195
	s_waitcnt lgkmcnt(0)
	s_barrier
; __device__ __forceinline__ unsigned f2bf(float f) { unsigned u = __builtin_bit_cast(unsigned, f); return (u + 0x7fffu + ((u >> 16) & 1u)) >> 16; }
; __device__ __forceinline__ int crow(int r, int hi) { return (r & 3) + 8 * (r >> 2) + 4 * hi; }
; #define ATT_WAIT_BAR() asm volatile("s_waitcnt vmcnt(0) lgkmcnt(0)\n\ts_barrier" ::: "memory")
; __device__ __forceinline__ void attn_dma_body(const bf16_t* __restrict__ Qb, int ldq, int tpos0, const float* __restrict__ rope, const float* __restrict__ qgain, ...
;     ...
;   if (hi == 0) li_l[r32] = l_reg; asm volatile("s_waitcnt lgkmcnt(0)" ::: "memory");
;   float rli[16];
; #pragma unroll
;   for (int r = 0; r < 16; ++r) rli[r] = __builtin_amdgcn_rcpf(li_l[crow(r, hi)]);
;   bf16_t* Ow = Ob + (long)(wid * QBLK) * LDO;
;   asm volatile("s_waitcnt lgkmcnt(0)\n\ts_barrier" ::: "memory");
;   { char* st = lds + wid * 8704;
; #pragma unroll
;     for (int r = 0; r < 16; ++r) { const int orow = crow(r, hi);
; #pragma unroll
;       for (int d0 = 0; d0 < 4; ++d0) *(bf16_t*)(st + orow * 272 + (d0 * 32 + r32) * 2) = (bf16_t)f2bf(o[d0][r] * rli[r]); }
;     asm volatile("s_waitcnt lgkmcnt(0)" ::: "memory");
; #pragma unroll
;     for (int i = 0; i < 8; ++i) { const int c = i * 64 + lane, row = c >> 4, cc = c & 15; const u32x4 v = *(const u32x4*)(st + row * 272 + cc * 16);
;       const bf16_t* gp = Ow + (long)row * LDO + cc * 8;
;       asm volatile("global_store_dwordx4 %0, %1, off sc1\n\ts_nop 1" :: "v"(gp), "v"(v) : "memory"); } }
;   ATT_WAIT_BAR();
	v_mul_u32_u24_e32 v84, 0x2200, v179
	v_and_b32_e32 v246, 15, v167
	v_lshrrev_b32_e32 v247, 4, v167
	v_mul_u32_u24_e32 v248, 0x110, v246
	v_add_u32_e32 v248, v248, v84
	v_lshl_add_u32 v248, v247, 3, v248
	v_mul_f32_e32 v2, v2, v182
	v_mul_f32_e32 v3, v3, v182
	v_mul_f32_e32 v4, v4, v182
	v_mul_f32_e32 v5, v5, v182
	v_cvt_pk_bf16_f32 v252, v2, v3
	v_cvt_pk_bf16_f32 v253, v4, v5
	ds_write_b64 v248, v[252:253] offset:0
	v_mul_f32_e32 v6, v6, v195
	v_mul_f32_e32 v7, v7, v195
	v_mul_f32_e32 v8, v8, v195
	v_mul_f32_e32 v9, v9, v195
	v_cvt_pk_bf16_f32 v254, v6, v7
	v_cvt_pk_bf16_f32 v255, v8, v9
	ds_write_b64 v248, v[254:255] offset:4352
	v_mul_f32_e32 v10, v10, v182
	v_mul_f32_e32 v11, v11, v182
	v_mul_f32_e32 v12, v12, v182
	v_mul_f32_e32 v13, v13, v182
	v_cvt_pk_bf16_f32 v252, v10, v11
	v_cvt_pk_bf16_f32 v253, v12, v13
	ds_write_b64 v248, v[252:253] offset:32
	v_mul_f32_e32 v14, v14, v195
	v_mul_f32_e32 v15, v15, v195
	v_mul_f32_e32 v16, v16, v195
	v_mul_f32_e32 v17, v17, v195
	v_cvt_pk_bf16_f32 v254, v14, v15
	v_cvt_pk_bf16_f32 v255, v16, v17
	ds_write_b64 v248, v[254:255] offset:4384
	v_mul_f32_e32 v18, v18, v182
	v_mul_f32_e32 v19, v19, v182
	v_mul_f32_e32 v20, v20, v182
	v_mul_f32_e32 v21, v21, v182
	v_cvt_pk_bf16_f32 v252, v18, v19
	v_cvt_pk_bf16_f32 v253, v20, v21
	ds_write_b64 v248, v[252:253] offset:64
	v_mul_f32_e32 v22, v22, v195
	v_mul_f32_e32 v23, v23, v195
	v_mul_f32_e32 v24, v24, v195
	v_mul_f32_e32 v25, v25, v195
	v_cvt_pk_bf16_f32 v254, v22, v23
	v_cvt_pk_bf16_f32 v255, v24, v25
	ds_write_b64 v248, v[254:255] offset:4416
	v_mul_f32_e32 v26, v26, v182
	v_mul_f32_e32 v27, v27, v182
	v_mul_f32_e32 v28, v28, v182
	v_mul_f32_e32 v29, v29, v182
	v_cvt_pk_bf16_f32 v252, v26, v27
	v_cvt_pk_bf16_f32 v253, v28, v29
	ds_write_b64 v248, v[252:253] offset:96
	v_mul_f32_e32 v30, v30, v195
	v_mul_f32_e32 v31, v31, v195
	v_mul_f32_e32 v32, v32, v195
	v_mul_f32_e32 v33, v33, v195
	v_cvt_pk_bf16_f32 v254, v30, v31
	v_cvt_pk_bf16_f32 v255, v32, v33
	ds_write_b64 v248, v[254:255] offset:4448
	v_mul_f32_e32 v34, v34, v182
	v_mul_f32_e32 v35, v35, v182
	v_mul_f32_e32 v36, v36, v182
	v_mul_f32_e32 v37, v37, v182
	v_cvt_pk_bf16_f32 v252, v34, v35
	v_cvt_pk_bf16_f32 v253, v36, v37
	ds_write_b64 v248, v[252:253] offset:128
	v_mul_f32_e32 v38, v38, v195
	v_mul_f32_e32 v39, v39, v195
	v_mul_f32_e32 v40, v40, v195
	v_mul_f32_e32 v41, v41, v195
	v_cvt_pk_bf16_f32 v254, v38, v39
	v_cvt_pk_bf16_f32 v255, v40, v41
	ds_write_b64 v248, v[254:255] offset:4480
	v_mul_f32_e32 v42, v42, v182
	v_mul_f32_e32 v43, v43, v182
	v_mul_f32_e32 v44, v44, v182
	v_mul_f32_e32 v45, v45, v182
	v_cvt_pk_bf16_f32 v252, v42, v43
	v_cvt_pk_bf16_f32 v253, v44, v45
	ds_write_b64 v248, v[252:253] offset:160
	v_mul_f32_e32 v46, v46, v195
	v_mul_f32_e32 v47, v47, v195
	v_mul_f32_e32 v48, v48, v195
	v_mul_f32_e32 v49, v49, v195
	v_cvt_pk_bf16_f32 v254, v46, v47
	v_cvt_pk_bf16_f32 v255, v48, v49
	ds_write_b64 v248, v[254:255] offset:4512
	v_mul_f32_e32 v50, v50, v182
	v_mul_f32_e32 v51, v51, v182
	v_mul_f32_e32 v52, v52, v182
	v_mul_f32_e32 v53, v53, v182
	v_cvt_pk_bf16_f32 v252, v50, v51
	v_cvt_pk_bf16_f32 v253, v52, v53
	ds_write_b64 v248, v[252:253] offset:192
	v_mul_f32_e32 v54, v54, v195
	v_mul_f32_e32 v55, v55, v195
	v_mul_f32_e32 v56, v56, v195
	v_mul_f32_e32 v57, v57, v195
	v_cvt_pk_bf16_f32 v254, v54, v55
	v_cvt_pk_bf16_f32 v255, v56, v57
	ds_write_b64 v248, v[254:255] offset:4544
	v_mul_f32_e32 v58, v58, v182
	v_mul_f32_e32 v59, v59, v182
	v_mul_f32_e32 v60, v60, v182
	v_mul_f32_e32 v61, v61, v182
	v_cvt_pk_bf16_f32 v252, v58, v59
	v_cvt_pk_bf16_f32 v253, v60, v61
	ds_write_b64 v248, v[252:253] offset:224
	v_mul_f32_e32 v62, v62, v195
	v_mul_f32_e32 v63, v63, v195
	v_mul_f32_e32 v64, v64, v195
	v_mul_f32_e32 v65, v65, v195
	v_cvt_pk_bf16_f32 v254, v62, v63
	v_cvt_pk_bf16_f32 v255, v64, v65
	ds_write_b64 v248, v[254:255] offset:4576
	s_waitcnt lgkmcnt(0)
	s_lshl_b64 s[6:7], s[70:71], 12
	s_add_u32 s6, s23, s6
	s_addc_u32 s7, s94, s7
	s_add_u32 s6, s6, s44
	s_addc_u32 s7, s7, s45
	v_ashrrev_i32_e32 v165, 31, v164
	v_lshlrev_b64 v[66:67], 12, v[164:165]
	v_lshl_add_u64 v[6:7], s[6:7], 0, v[66:67]
	v_lshlrev_b32_e32 v162, 4, v246
	v_lshl_add_u64 v[6:7], v[6:7], 0, v[162:163]
	v_lshlrev_b32_e32 v162, 12, v247
	v_lshl_add_u64 v[6:7], v[6:7], 0, v[162:163]
	v_mul_u32_u24_e32 v249, 0x110, v247
	v_add_u32_e32 v249, v249, v84
	v_lshl_add_u32 v249, v246, 4, v249
	ds_read_b128 v[10:13], v249 offset:0
	s_mov_b64 s[8:9], 0x0
	v_lshl_add_u64 v[8:9], v[6:7], 0, s[8:9]
	s_waitcnt lgkmcnt(0)
	global_store_dwordx4 v[8:9], v[10:13], off sc1
	s_nop 1
	ds_read_b128 v[14:17], v249 offset:1088
	s_mov_b64 s[8:9], 0x4000
	v_lshl_add_u64 v[8:9], v[6:7], 0, s[8:9]
	s_waitcnt lgkmcnt(0)
	global_store_dwordx4 v[8:9], v[14:17], off sc1
	s_nop 1
	ds_read_b128 v[10:13], v249 offset:2176
	s_mov_b64 s[8:9], 0x8000
	v_lshl_add_u64 v[8:9], v[6:7], 0, s[8:9]
	s_waitcnt lgkmcnt(0)
	global_store_dwordx4 v[8:9], v[10:13], off sc1
	s_nop 1
	ds_read_b128 v[14:17], v249 offset:3264
	s_mov_b64 s[8:9], 0xc000
	v_lshl_add_u64 v[8:9], v[6:7], 0, s[8:9]
	s_waitcnt lgkmcnt(0)
	global_store_dwordx4 v[8:9], v[14:17], off sc1
	s_nop 1
	ds_read_b128 v[10:13], v249 offset:4352
	s_mov_b64 s[8:9], 0x10000
	v_lshl_add_u64 v[8:9], v[6:7], 0, s[8:9]
	s_waitcnt lgkmcnt(0)
	global_store_dwordx4 v[8:9], v[10:13], off sc1
	s_nop 1
	ds_read_b128 v[14:17], v249 offset:5440
	s_mov_b64 s[8:9], 0x14000
	v_lshl_add_u64 v[8:9], v[6:7], 0, s[8:9]
	s_waitcnt lgkmcnt(0)
	global_store_dwordx4 v[8:9], v[14:17], off sc1
	s_nop 1
	ds_read_b128 v[10:13], v249 offset:6528
	s_mov_b64 s[8:9], 0x18000
	v_lshl_add_u64 v[8:9], v[6:7], 0, s[8:9]
	s_waitcnt lgkmcnt(0)
	global_store_dwordx4 v[8:9], v[10:13], off sc1
	s_nop 1
	ds_read_b128 v[14:17], v249 offset:7616
	s_mov_b64 s[8:9], 0x1c000
	v_lshl_add_u64 v[8:9], v[6:7], 0, s[8:9]
	s_waitcnt lgkmcnt(0)
	global_store_dwordx4 v[8:9], v[14:17], off sc1
	s_nop 1
	s_waitcnt vmcnt(0) lgkmcnt(0)
	s_barrier
	v_readlane_b32 s96, v250, 4
	v_readlane_b32 s97, v250, 5
	s_setprio 0
	s_branch .LBB0_437
